# topk VALU trims: rank counting skips the two -inf filler entries per head; magic adds on aligned pairs packed into v_pk_add_f32
# speedup vs baseline: 1.0056x; 1.0056x over previous
.LBB0_1844:
	v_readlane_b32 s0, v253, 60
	v_readlane_b32 s1, v253, 61
	s_andn2_b64 vcc, exec, s[0:1]
	s_cbranch_vccnz .LBB0_1876
	v_and_b32_e32 v33, -8, v32
	v_cmp_eq_u32_e64 s[44:45], 16, v33
	v_subrev_u32_e32 v46, 24, v32
	v_subrev_u32_e32 v47, 29, v32
	v_cndmask_b32_e64 v51, 0, 4, s[44:45]
	v_cmp_lt_u32_e64 s[44:45], 4, v46
	v_subrev_u32_e32 v48, 33, v32
	v_and_b32_e32 v49, -2, v32
	v_cndmask_b32_e64 v46, 8, v51, s[44:45]
	v_cmp_lt_u32_e64 s[44:45], 3, v47
	v_cmp_eq_u32_e32 vcc, 1, v32
	s_mov_b32 s0, s38
	v_cndmask_b32_e64 v46, 12, v46, s[44:45]
	v_cmp_lt_u32_e64 s[44:45], 2, v48
	v_writelane_b32 v255, s0, 45
	v_readlane_b32 s8, v251, 38
	v_cndmask_b32_e64 v46, 16, v46, s[44:45]
	v_cmp_ne_u32_e64 s[44:45], 36, v49
	v_writelane_b32 v255, s1, 46
	v_lshlrev_b32_e32 v44, 4, v32
	v_cndmask_b32_e64 v46, 20, v46, s[44:45]
	v_cmp_ne_u32_e64 s[44:45], 38, v49
	v_readlane_b32 s9, v251, 39
	v_lshlrev_b32_e32 v36, 5, v32
	v_cndmask_b32_e64 v46, 24, v46, s[44:45]
	v_cmp_ne_u32_e64 s[44:45], 40, v49
	v_lshlrev_b32_e32 v38, 3, v32
	v_add_u32_e32 v42, 0x400, v44
	v_cndmask_b32_e64 v46, 28, v46, s[44:45]
	v_cmp_ne_u32_e64 s[44:45], 42, v32
	v_readlane_b32 s8, v255, 4
	v_ashrrev_i32_e32 v37, 31, v36
	v_cndmask_b32_e64 v46, 32, v46, s[44:45]
	v_cmp_ne_u32_e64 s[44:45], 43, v32
	v_and_b32_e32 v139, 0x78, v38
	v_and_b32_e32 v100, 0xffffff80, v38
	v_cndmask_b32_e64 v46, 36, v46, s[44:45]
	v_cmp_ne_u32_e64 s[44:45], 44, v32
	v_ashrrev_i32_e32 v38, 3, v32
	v_ashrrev_i32_e32 v42, 7, v42
	v_cndmask_b32_e64 v46, 40, v46, s[44:45]
	v_cmp_ne_u32_e64 s[44:45], 45, v32
	v_readlane_b32 s9, v255, 5
	s_lshl_b32 s4, s38, 11
	v_cndmask_b32_e64 v46, 44, v46, s[44:45]
	v_cmp_ne_u32_e64 s[44:45], 46, v32
	v_ashrrev_i32_e32 v39, 31, v38
	v_ashrrev_i32_e32 v43, 31, v42
	v_cndmask_b32_e64 v46, 48, v46, s[44:45]
	v_cmp_ne_u32_e64 s[44:45], 47, v32
	v_lshl_add_u64 v[122:123], s[8:9], 0, v[36:37]
	v_readlane_b32 s8, v255, 10
	v_cndmask_b32_e64 v46, 52, v46, s[44:45]
	v_cmp_ne_u32_e64 s[44:45], 48, v32
	s_cmp_lg_u32 s38, 3
	v_lshlrev_b64 v[40:41], 21, v[38:39]
	v_cndmask_b32_e64 v46, 56, v46, s[44:45]
	v_cmp_ne_u32_e64 s[44:45], 49, v32
	v_lshlrev_b64 v[42:43], 21, v[42:43]
	v_readlane_b32 s9, v255, 11
	v_cndmask_b32_e64 v146, 60, v46, s[44:45]
	v_cndmask_b32_e64 v46, 0, 4, vcc
	v_cmp_ne_u32_e32 vcc, 2, v32
	s_cselect_b64 s[68:69], -1, 0
	s_add_i32 s94, s4, 0x800
	v_cndmask_b32_e32 v46, 8, v46, vcc
	v_cmp_ne_u32_e32 vcc, 3, v32
	v_lshl_add_u64 v[124:125], s[8:9], 0, v[42:43]
	v_lshl_add_u64 v[126:127], s[8:9], 0, v[40:41]
	v_cndmask_b32_e32 v46, 12, v46, vcc
	v_cmp_ne_u32_e32 vcc, 4, v32
	v_readlane_b32 s8, v255, 18
	s_mov_b64 s[62:63], s[52:53]
	v_cndmask_b32_e32 v46, 16, v46, vcc
	v_cmp_ne_u32_e32 vcc, 5, v32
	s_lshl_b64 s[52:53], s[94:95], 2
	v_readlane_b32 s20, v251, 50
	v_cndmask_b32_e32 v46, 20, v46, vcc
	v_cmp_ne_u32_e32 vcc, 6, v32
	v_readlane_b32 s9, v255, 19
	v_subrev_u32_e32 v50, 42, v32
	v_cndmask_b32_e32 v46, 24, v46, vcc
	v_cmp_ne_u32_e32 vcc, 7, v32
	v_ashrrev_i32_e32 v33, 31, v32
	v_ashrrev_i32_e32 v45, 31, v44
	v_cndmask_b32_e32 v46, 28, v46, vcc
	v_cmp_ne_u32_e32 vcc, 8, v32
	v_readlane_b32 s21, v251, 51
	s_add_u32 s52, s20, s52
	v_cndmask_b32_e32 v46, 32, v46, vcc
	v_cmp_ne_u32_e32 vcc, 9, v32
	v_lshl_add_u64 v[128:129], s[8:9], 0, v[42:43]
	v_lshl_add_u64 v[130:131], s[8:9], 0, v[40:41]
	v_cndmask_b32_e32 v46, 36, v46, vcc
	v_cmp_ne_u32_e32 vcc, 10, v32
	v_readlane_b32 s8, v255, 24
	v_lshlrev_b64 v[34:35], 2, v[32:33]
	v_cndmask_b32_e32 v46, 40, v46, vcc
	v_cmp_ne_u32_e32 vcc, 11, v32
	v_ashrrev_i32_e32 v33, 4, v32
	s_addc_u32 s53, s21, s53
	v_cndmask_b32_e32 v46, 44, v46, vcc
	v_cmp_ne_u32_e32 vcc, 12, v32
	v_lshlrev_b64 v[110:111], 2, v[44:45]
	v_readlane_b32 s9, v255, 25
	v_cndmask_b32_e32 v46, 48, v46, vcc
	v_cmp_ne_u32_e32 vcc, 13, v32
	v_cmp_gt_u32_e64 s[4:5], 50, v32
	v_cmp_eq_u32_e64 s[78:79], 0, v32
	v_cndmask_b32_e32 v46, 52, v46, vcc
	v_cmp_ne_u32_e32 vcc, 14, v32
	v_cmp_gt_i32_e64 s[76:77], 32, v32
	v_and_b32_e32 v140, 15, v32
	v_cndmask_b32_e32 v46, 56, v46, vcc
	v_cmp_ne_u32_e32 vcc, 15, v32
	v_sub_u32_e32 v141, 63, v32
	v_lshl_add_u32 v142, v32, 2, s84
	v_cndmask_b32_e32 v46, 60, v46, vcc
	v_cmp_ne_u32_e32 vcc, 16, v32
	v_cmp_gt_u32_e64 s[44:45], 16, v32
	v_cmp_eq_u32_e64 s[46:47], 1, v33
	v_cndmask_b32_e32 v46, 0, v46, vcc
	v_cmp_ne_u32_e32 vcc, 17, v32
	v_cmp_eq_u32_e64 s[48:49], 2, v33
	v_cmp_eq_u32_e64 s[50:51], 3, v33
	v_cndmask_b32_e32 v46, 4, v46, vcc
	v_cmp_ne_u32_e32 vcc, 18, v32
	v_add_u32_e32 v33, 64, v32
	v_lshl_add_u64 v[112:113], s[52:53], 0, v[110:111]
	v_cndmask_b32_e32 v46, 8, v46, vcc
	v_cmp_ne_u32_e32 vcc, 19, v32
	s_mov_b64 s[52:53], 0x1010
	v_lshl_add_u64 v[132:133], s[8:9], 0, v[34:35]
	v_cndmask_b32_e32 v46, 12, v46, vcc
	v_cmp_ne_u32_e32 vcc, 20, v32
	v_readlane_b32 s8, v255, 26
	v_readlane_b32 s18, v251, 48
	v_cndmask_b32_e32 v46, 16, v46, vcc
	v_cmp_ne_u32_e32 vcc, 21, v32
	v_readlane_b32 s19, v251, 49
	v_readlane_b32 s22, v251, 52
	v_cndmask_b32_e32 v46, 20, v46, vcc
	v_cmp_ne_u32_e32 vcc, 22, v32
	v_readlane_b32 s23, v251, 53
	v_lshl_add_u64 v[116:117], v[112:113], 0, s[52:53]
	v_cndmask_b32_e32 v46, 24, v46, vcc
	v_cmp_ne_u32_e32 vcc, 23, v32
	s_mov_b64 s[52:53], 0x1020
	v_readlane_b32 s9, v255, 27
	v_cndmask_b32_e32 v46, 28, v46, vcc
	v_cmp_ne_u32_e32 vcc, 24, v32
	v_lshlrev_b32_e32 v200, 1, v139
	v_add_u32_e32 v104, 0x200, v100
	v_cndmask_b32_e32 v46, 0, v46, vcc
	v_cmp_ne_u32_e32 vcc, 25, v32
	v_add_u32_e32 v106, 0x400, v100
	v_add_u32_e32 v108, 0x600, v100
	v_cndmask_b32_e32 v46, 4, v46, vcc
	v_cmp_ne_u32_e32 vcc, 26, v32
	v_readlane_b32 s12, v251, 42
	v_readlane_b32 s13, v251, 43
	v_cndmask_b32_e32 v46, 8, v46, vcc
	v_cmp_ne_u32_e32 vcc, 27, v32
	v_readlane_b32 s14, v251, 44
	v_readlane_b32 s15, v251, 45
	v_cndmask_b32_e32 v46, 12, v46, vcc
	v_cmp_ne_u32_e32 vcc, 28, v32
	s_mov_b64 s[22:23], s[76:77]
	s_mov_b64 s[18:19], s[68:69]
	v_cndmask_b32_e32 v46, 16, v46, vcc
	v_cmp_ne_u32_e32 vcc, 29, v32
	v_lshl_add_u64 v[118:119], v[112:113], 0, s[52:53]
	s_mov_b64 s[52:53], 0x1030
	v_cndmask_b32_e32 v46, 0, v46, vcc
	v_cmp_ne_u32_e32 vcc, 30, v32
	v_readlane_b32 s68, v255, 16
	v_readlane_b32 s76, v254, 62
	v_cndmask_b32_e32 v46, 4, v46, vcc
	v_cmp_ne_u32_e32 vcc, 31, v32
	s_waitcnt vmcnt(0)
	v_lshl_add_u64 v[96:97], s[66:67], 0, v[34:35]
	v_lshl_add_u64 v[98:99], v[36:37], 1, s[70:71]
	v_cndmask_b32_e32 v46, 8, v46, vcc
	v_cmp_ne_u32_e32 vcc, 32, v32
	v_lshl_add_u64 v[102:103], s[96:97], 0, v[200:201]
	v_and_b32_e32 v200, 0x70, v44
	v_cndmask_b32_e32 v46, 12, v46, vcc
	v_cmp_ne_u32_e32 vcc, 33, v32
	v_or_b32_e32 v143, 1, v139
	v_or_b32_e32 v144, 2, v139
	v_cndmask_b32_e32 v46, 0, v46, vcc
	v_cmp_ne_u32_e32 vcc, 34, v32
	v_or_b32_e32 v145, 3, v139
	v_ashrrev_i32_e32 v101, 31, v100
	v_cndmask_b32_e32 v46, 4, v46, vcc
	v_cmp_ne_u32_e32 vcc, 35, v32
	v_ashrrev_i32_e32 v105, 31, v104
	v_ashrrev_i32_e32 v107, 31, v106
	v_cndmask_b32_e32 v46, 8, v46, vcc
	v_cmp_ne_u32_e32 vcc, 36, v32
	v_ashrrev_i32_e32 v109, 31, v108
	v_cmp_eq_u32_e64 s[0:1], 0, v140
	v_cndmask_b32_e32 v46, 0, v46, vcc
	v_cmp_ne_u32_e32 vcc, 37, v32
	v_cmp_eq_u32_e64 s[54:55], 1, v140
	v_cmp_eq_u32_e64 s[64:65], 2, v140
	v_cndmask_b32_e32 v46, 4, v46, vcc
	v_cmp_ne_u32_e32 vcc, 38, v32
	v_cmp_eq_u32_e64 s[2:3], 3, v140
	v_cmp_eq_u32_e64 s[6:7], 4, v140
	v_cndmask_b32_e32 v46, 0, v46, vcc
	v_cmp_ne_u32_e32 vcc, 39, v32
	v_cmp_eq_u32_e64 s[96:97], 5, v140
	v_cmp_eq_u32_e64 s[66:67], 6, v140
	v_cndmask_b32_e32 v46, 4, v46, vcc
	v_cmp_ne_u32_e32 vcc, 40, v32
	v_cmp_eq_u32_e64 s[24:25], 7, v140
	v_cmp_eq_u32_e64 s[26:27], 8, v140
	v_cndmask_b32_e32 v46, 0, v46, vcc
	v_cmp_ne_u32_e32 vcc, 41, v32
	v_and_b32_e32 v32, 7, v32
	v_lshlrev_b32_e32 v32, 6, v32
	v_cndmask_b32_e32 v46, 4, v46, vcc
	v_cmp_lt_u32_e32 vcc, 7, v50
	v_cmp_eq_u32_e64 s[28:29], 9, v140
	v_cmp_eq_u32_e64 s[30:31], 10, v140
	v_cndmask_b32_e32 v46, 0, v46, vcc
	v_add_u32_e32 v147, 64, v46
	v_add_u32_e32 v149, 0xc0, v46
	v_ashrrev_i32_e32 v46, 3, v33
	v_mov_b32_e32 v33, v201
	v_ashrrev_i32_e32 v47, 31, v46
	v_lshl_add_u64 v[32:33], s[8:9], 0, v[32:33]
	v_cmp_eq_u32_e64 s[34:35], 11, v140
	v_cmp_eq_u32_e64 s[36:37], 12, v140
	v_cmp_eq_u32_e64 s[38:39], 13, v140
	v_cmp_eq_u32_e64 s[40:41], 14, v140
	v_cmp_eq_u32_e64 s[42:43], 15, v140
	v_add_u32_e32 v148, 0x80, v146
	v_or_b32_e32 v150, 16, v140
	v_or_b32_e32 v151, 32, v140
	v_or_b32_e32 v152, 48, v140
	s_mov_b64 s[20:21], s[78:79]
	v_lshl_add_u64 v[114:115], v[112:113], 0, s[60:61]
	v_lshl_add_u64 v[120:121], v[112:113], 0, s[52:53]
	v_lshl_add_u64 v[134:135], v[38:39], 2, v[32:33]
	v_lshl_add_u64 v[136:137], v[46:47], 2, v[32:33]
	v_readlane_b32 s69, v255, 17
	s_mov_b64 s[14:15], s[62:63]
	s_mov_b64 s[12:13], s[74:75]
	v_readlane_b32 s77, v254, 63
	s_mov_b32 s8, s80
	v_readlane_b32 s10, v251, 40
	v_readlane_b32 s11, v251, 41
	v_readlane_b32 s16, v251, 46
	v_readlane_b32 s17, v251, 47
	v_mov_b32_e32 v226, 0x30c0400
	v_mov_b32_e32 v228, 0x3040100
	v_mov_b32_e32 v242, 0x4b400000
	s_branch .LBB0_1848

.LBB0_1850:
	s_or_b64 exec, exec, s[52:53]
	v_lshlrev_b32_e32 v154, 16, v28
	v_and_b32_e32 v155, 0xffff0000, v28
	v_lshlrev_b32_e32 v28, 16, v29
	v_and_b32_e32 v29, 0xffff0000, v29
	v_pk_mul_f32 v[154:155], v[138:139], v[154:155] op_sel_hi:[0,1]
	v_pk_mul_f32 v[28:29], v[138:139], v[28:29] op_sel_hi:[0,1]
	v_med3_f32 v153, v154, s88, v236
	v_med3_f32 v154, v155, s88, v236
	v_med3_f32 v28, v28, s88, v236
	v_med3_f32 v29, v29, s88, v236
	v_add_f32_e32 v154, 0x4b400000, v154
	v_add_f32_e32 v153, 0x4b400000, v153
	v_pk_add_f32 v[28:29], v[28:29], v[242:243] op_sel_hi:[1,0]
	s_mov_b32 s9, 0x40c0c00
	v_perm_b32 v29, v29, v153, s9
	v_perm_b32 v230, v154, v29, v226
	v_perm_b32 v28, v28, v230, v228
	v_lshlrev_b32_e32 v154, 16, v30
	v_and_b32_e32 v155, 0xffff0000, v30
	v_lshlrev_b32_e32 v30, 16, v31
	v_and_b32_e32 v31, 0xffff0000, v31
	v_pk_mul_f32 v[154:155], v[138:139], v[154:155] op_sel_hi:[0,1]
	v_pk_mul_f32 v[30:31], v[138:139], v[30:31] op_sel_hi:[0,1]
	v_med3_f32 v153, v155, s88, v236
	v_med3_f32 v29, v154, s88, v236
	v_med3_f32 v30, v30, s88, v236
	v_med3_f32 v31, v31, s88, v236
	v_add_f32_e32 v153, 0x4b400000, v153
	v_add_f32_e32 v29, 0x4b400000, v29
	v_pk_add_f32 v[30:31], v[30:31], v[242:243] op_sel_hi:[1,0]
	v_perm_b32 v29, v31, v29, s9
	v_perm_b32 v230, v153, v29, v226
	v_perm_b32 v29, v30, v230, v228
	v_lshlrev_b32_e32 v30, 16, v24
	v_and_b32_e32 v31, 0xffff0000, v24
	v_lshlrev_b32_e32 v24, 16, v25
	v_and_b32_e32 v25, 0xffff0000, v25
	v_pk_mul_f32 v[30:31], v[138:139], v[30:31] op_sel_hi:[0,1]
	v_pk_mul_f32 v[24:25], v[138:139], v[24:25] op_sel_hi:[0,1]
	v_med3_f32 v31, v31, s88, v236
	v_med3_f32 v30, v30, s88, v236
	v_med3_f32 v24, v24, s88, v236
	v_med3_f32 v25, v25, s88, v236
	v_pk_add_f32 v[30:31], v[30:31], v[242:243] op_sel_hi:[1,0]
	v_pk_add_f32 v[24:25], v[24:25], v[242:243] op_sel_hi:[1,0]
	v_perm_b32 v25, v25, v30, s9
	v_perm_b32 v230, v31, v25, v226
	v_perm_b32 v30, v24, v230, v228
	v_lshlrev_b32_e32 v24, 16, v26
	v_and_b32_e32 v25, 0xffff0000, v26
	v_lshlrev_b32_e32 v26, 16, v27
	v_and_b32_e32 v27, 0xffff0000, v27
	v_pk_mul_f32 v[24:25], v[138:139], v[24:25] op_sel_hi:[0,1]
	v_pk_mul_f32 v[26:27], v[138:139], v[26:27] op_sel_hi:[0,1]
	v_med3_f32 v25, v25, s88, v236
	v_med3_f32 v24, v24, s88, v236
	v_med3_f32 v26, v26, s88, v236
	v_med3_f32 v27, v27, s88, v236
	v_pk_add_f32 v[24:25], v[24:25], v[242:243] op_sel_hi:[1,0]
	v_pk_add_f32 v[26:27], v[26:27], v[242:243] op_sel_hi:[1,0]
	v_perm_b32 v24, v27, v24, s9
	v_perm_b32 v230, v25, v24, v226
	v_perm_b32 v31, v26, v230, v228
	v_lshlrev_b32_e32 v24, 16, v20
	v_and_b32_e32 v25, 0xffff0000, v20
	v_lshlrev_b32_e32 v20, 16, v21
	v_and_b32_e32 v21, 0xffff0000, v21
	v_pk_mul_f32 v[24:25], v[138:139], v[24:25] op_sel_hi:[0,1]
	v_pk_mul_f32 v[20:21], v[138:139], v[20:21] op_sel_hi:[0,1]
	v_med3_f32 v25, v25, s88, v236
	v_med3_f32 v24, v24, s88, v236
	v_med3_f32 v20, v20, s88, v236
	v_med3_f32 v21, v21, s88, v236
	v_pk_add_f32 v[24:25], v[24:25], v[242:243] op_sel_hi:[1,0]
	v_pk_add_f32 v[20:21], v[20:21], v[242:243] op_sel_hi:[1,0]
	v_perm_b32 v21, v21, v24, s9
	v_perm_b32 v230, v25, v21, v226
	v_perm_b32 v20, v20, v230, v228
	v_lshlrev_b32_e32 v24, 16, v22
	v_and_b32_e32 v25, 0xffff0000, v22
	v_lshlrev_b32_e32 v22, 16, v23
	v_and_b32_e32 v23, 0xffff0000, v23
	v_pk_mul_f32 v[24:25], v[138:139], v[24:25] op_sel_hi:[0,1]
	v_pk_mul_f32 v[22:23], v[138:139], v[22:23] op_sel_hi:[0,1]
	v_med3_f32 v21, v24, s88, v236
	v_med3_f32 v24, v25, s88, v236
	v_med3_f32 v22, v22, s88, v236
	v_med3_f32 v23, v23, s88, v236
	v_add_f32_e32 v24, 0x4b400000, v24
	v_add_f32_e32 v21, 0x4b400000, v21
	v_pk_add_f32 v[22:23], v[22:23], v[242:243] op_sel_hi:[1,0]
	v_perm_b32 v21, v23, v21, s9
	v_perm_b32 v230, v24, v21, v226
	v_perm_b32 v21, v22, v230, v228
	v_lshlrev_b32_e32 v22, 16, v16
	v_and_b32_e32 v23, 0xffff0000, v16
	v_lshlrev_b32_e32 v16, 16, v17
	v_and_b32_e32 v17, 0xffff0000, v17
	v_pk_mul_f32 v[22:23], v[138:139], v[22:23] op_sel_hi:[0,1]
	v_pk_mul_f32 v[16:17], v[138:139], v[16:17] op_sel_hi:[0,1]
	v_med3_f32 v23, v23, s88, v236
	v_med3_f32 v22, v22, s88, v236
	v_med3_f32 v16, v16, s88, v236
	v_med3_f32 v17, v17, s88, v236
	v_pk_add_f32 v[22:23], v[22:23], v[242:243] op_sel_hi:[1,0]
	v_pk_add_f32 v[16:17], v[16:17], v[242:243] op_sel_hi:[1,0]
	v_perm_b32 v17, v17, v22, s9
	v_perm_b32 v230, v23, v17, v226
	v_perm_b32 v22, v16, v230, v228
	v_lshlrev_b32_e32 v16, 16, v18
	v_and_b32_e32 v17, 0xffff0000, v18
	v_lshlrev_b32_e32 v18, 16, v19
	v_and_b32_e32 v19, 0xffff0000, v19
	v_pk_mul_f32 v[16:17], v[138:139], v[16:17] op_sel_hi:[0,1]
	v_pk_mul_f32 v[18:19], v[138:139], v[18:19] op_sel_hi:[0,1]
	v_med3_f32 v17, v17, s88, v236
	v_med3_f32 v16, v16, s88, v236
	v_med3_f32 v18, v18, s88, v236
	v_med3_f32 v19, v19, s88, v236
	v_pk_add_f32 v[16:17], v[16:17], v[242:243] op_sel_hi:[1,0]
	s_nop 0
	v_pk_add_f32 v[18:19], v[18:19], v[242:243] op_sel_hi:[1,0]
	s_nop 0
	s_nop 0
	s_nop 0
	v_readlane_b32 s10, v255, 20
	s_nop 0
	s_add_i32 s94, s80, s10
	s_nop 0
	s_nop 0
	v_perm_b32 v16, v19, v16, s9
	s_cmpk_gt_i32 s94, 0x3fff
	v_perm_b32 v230, v17, v16, v226
	v_perm_b32 v23, v18, v230, v228
	v_lshl_add_u64 v[16:17], s[92:93], 0, v[122:123]
	s_mov_b32 s52, 0x33200000
	s_cselect_b64 s[78:79], -1, 0
	s_cmpk_lt_i32 s94, 0x4000
	v_add_co_u32_e32 v16, vcc, s52, v16
	s_cselect_b32 s52, s94, s80
	s_nop 0
	v_addc_co_u32_e32 v17, vcc, 0, v17, vcc
	s_ashr_i32 s53, s52, 31
	v_mov_b32_e32 v138, 0
	global_store_dwordx4 v[16:17], v[28:31], off
	global_store_dwordx4 v[16:17], v[20:23], off offset:16
	v_readlane_b32 s11, v255, 21
	s_and_saveexec_b64 s[80:81], s[22:23]
	s_cbranch_execz .LBB0_1852
	s_lshl_b64 vcc, s[52:53], 7
	v_lshl_add_u64 v[16:17], v[96:97], 0, vcc
	global_load_dword v138, v[16:17], off

.LBB0_1854:
	v_cndmask_b32_e64 v153, 0, v153, s[0:1]
	v_cndmask_b32_e64 v154, 0, v154, s[0:1]
	v_cndmask_b32_e64 v153, v153, v157, s[54:55]
	v_cndmask_b32_e64 v155, 0, v155, s[0:1]
	v_cndmask_b32_e64 v154, v154, v158, s[54:55]
	v_cndmask_b32_e64 v153, v153, v161, s[64:65]
	v_cndmask_b32_e64 v155, v155, v159, s[54:55]
	v_cndmask_b32_e64 v154, v154, v162, s[64:65]
	v_cndmask_b32_e64 v153, v153, v165, s[2:3]
	v_cndmask_b32_e64 v155, v155, v163, s[64:65]
	v_cndmask_b32_e64 v154, v154, v166, s[2:3]
	v_cndmask_b32_e64 v153, v153, v169, s[6:7]
	v_cndmask_b32_e64 v155, v155, v167, s[2:3]
	v_cndmask_b32_e64 v154, v154, v170, s[6:7]
	v_cndmask_b32_e64 v153, v153, v173, s[96:97]
	v_cndmask_b32_e64 v156, 0, v156, s[0:1]
	v_cndmask_b32_e64 v155, v155, v171, s[6:7]
	v_cndmask_b32_e64 v154, v154, v174, s[96:97]
	v_cndmask_b32_e64 v153, v153, v177, s[66:67]
	v_cndmask_b32_e64 v156, v156, v160, s[54:55]
	v_cndmask_b32_e64 v155, v155, v175, s[96:97]
	v_cndmask_b32_e64 v154, v154, v178, s[66:67]
	v_cndmask_b32_e64 v153, v153, v181, s[24:25]
	v_cndmask_b32_e64 v156, v156, v164, s[64:65]
	v_cndmask_b32_e64 v155, v155, v179, s[66:67]
	v_cndmask_b32_e64 v154, v154, v182, s[24:25]
	v_cndmask_b32_e64 v153, v153, v185, s[26:27]
	v_cndmask_b32_e64 v156, v156, v168, s[2:3]
	v_cndmask_b32_e64 v155, v155, v183, s[24:25]
	v_cndmask_b32_e64 v154, v154, v186, s[26:27]
	v_cndmask_b32_e64 v153, v153, v189, s[28:29]
	v_cndmask_b32_e64 v156, v156, v172, s[6:7]
	v_cndmask_b32_e64 v155, v155, v187, s[26:27]
	v_cndmask_b32_e64 v154, v154, v190, s[28:29]
	v_cndmask_b32_e64 v153, v153, v193, s[30:31]
	v_cndmask_b32_e64 v156, v156, v176, s[96:97]
	v_cndmask_b32_e64 v155, v155, v191, s[28:29]
	v_cndmask_b32_e64 v154, v154, v194, s[30:31]
	v_cndmask_b32_e64 v153, v153, v197, s[34:35]
	v_cndmask_b32_e64 v156, v156, v180, s[66:67]
	v_cndmask_b32_e64 v155, v155, v195, s[30:31]
	v_cndmask_b32_e64 v154, v154, v198, s[34:35]
	v_cndmask_b32_e64 v153, v153, v206, s[36:37]
	v_cndmask_b32_e64 v156, v156, v184, s[24:25]
	v_cndmask_b32_e64 v155, v155, v199, s[34:35]
	v_cndmask_b32_e64 v154, v154, v207, s[36:37]
	v_cndmask_b32_e64 v153, v153, v210, s[38:39]
	v_cndmask_b32_e64 v156, v156, v188, s[26:27]
	v_cndmask_b32_e64 v155, v155, v208, s[36:37]
	v_cndmask_b32_e64 v154, v154, v211, s[38:39]
	v_cndmask_b32_e64 v153, v153, v214, s[40:41]
	v_max_i32_e32 v157, v218, v219
	v_cndmask_b32_e64 v156, v156, v192, s[28:29]
	v_cndmask_b32_e64 v155, v155, v212, s[38:39]
	v_cndmask_b32_e64 v154, v154, v215, s[40:41]
	v_cndmask_b32_e64 v153, v153, v157, s[42:43]
	v_max_i32_e32 v157, v220, v221
	v_cndmask_b32_e64 v156, v156, v196, s[30:31]
	v_cndmask_b32_e64 v155, v155, v216, s[40:41]
	v_cndmask_b32_e64 v157, v154, v157, s[42:43]
	v_max_i32_e32 v154, v240, v241
	ds_bpermute_b32 v158, v146, v153
	v_cndmask_b32_e64 v156, v156, v203, s[34:35]
	v_cndmask_b32_e64 v159, v155, v154, s[42:43]
	ds_bpermute_b32 v154, v147, v153
	v_cndmask_b32_e64 v156, v156, v209, s[36:37]
	v_cndmask_b32_e64 v156, v156, v213, s[38:39]
	v_cndmask_b32_e64 v156, v156, v217, s[40:41]
	v_max_i32_e32 v155, v222, v223
	v_cndmask_b32_e64 v167, v156, v155, s[42:43]
	s_waitcnt lgkmcnt(1)
	v_lshlrev_b32_e32 v155, 7, v158
	v_and_b32_e32 v155, 0x3f80, v155
	s_waitcnt lgkmcnt(0)
	v_and_b32_e32 v156, 0x7f, v154
	s_movk_i32 s9, 0x3fff
	v_bitop3_b32 v184, v156, s9, v155 bitop3:0x36
	v_ashrrev_i32_e32 v155, 31, v154
	v_ashrrev_i32_e32 v156, 31, v158
	v_and_b32_e32 v155, 0x7fffffff, v155
	v_and_b32_e32 v156, 0x7fffffff, v156
	v_xor_b32_e32 v155, v155, v154
	v_xor_b32_e32 v154, v156, v158
	ds_bpermute_b32 v156, v148, v153
	ds_bpermute_b32 v153, v149, v153
	v_pk_add_f32 v[154:155], v[154:155], v[154:155] op_sel:[1,0] op_sel_hi:[0,1]
	s_movk_i32 s10, 0xffc0
	v_and_or_b32 v154, v154, s10, v141
	v_cndmask_b32_e64 v185, v238, v154, s[4:5]
	s_waitcnt lgkmcnt(1)
	v_lshlrev_b32_e32 v154, 7, v156
	v_and_b32_e32 v154, 0x3f80, v154
	s_waitcnt lgkmcnt(0)
	v_and_b32_e32 v155, 0x7f, v153
	v_bitop3_b32 v166, v155, s9, v154 bitop3:0x36
	v_ashrrev_i32_e32 v154, 31, v153
	v_ashrrev_i32_e32 v155, 31, v156
	v_and_b32_e32 v154, 0x7fffffff, v154
	v_and_b32_e32 v158, 0x7fffffff, v155
	v_xor_b32_e32 v155, v154, v153
	v_xor_b32_e32 v154, v158, v156
	v_pk_add_f32 v[154:155], v[154:155], v[154:155] op_sel:[1,0] op_sel_hi:[0,1]
	ds_bpermute_b32 v153, v146, v157
	ds_bpermute_b32 v155, v147, v157
	v_and_or_b32 v154, v154, s10, v141
	v_cndmask_b32_e64 v186, v238, v154, s[4:5]
	ds_bpermute_b32 v187, v149, v167
	s_waitcnt lgkmcnt(2)
	v_lshlrev_b32_e32 v154, 7, v153
	v_and_b32_e32 v154, 0x3f80, v154
	s_waitcnt lgkmcnt(1)
	v_and_b32_e32 v156, 0x7f, v155
	v_bitop3_b32 v164, v156, s9, v154 bitop3:0x36
	v_ashrrev_i32_e32 v154, 31, v155
	v_ashrrev_i32_e32 v156, 31, v153
	v_and_b32_e32 v154, 0x7fffffff, v154
	v_and_b32_e32 v156, 0x7fffffff, v156
	v_xor_b32_e32 v155, v154, v155
	v_xor_b32_e32 v154, v156, v153
	ds_bpermute_b32 v153, v148, v157
	v_pk_add_f32 v[154:155], v[154:155], v[154:155] op_sel:[1,0] op_sel_hi:[0,1]
	ds_bpermute_b32 v155, v149, v157
	v_and_or_b32 v154, v154, s10, v141
	v_cndmask_b32_e64 v165, v238, v154, s[4:5]
	s_waitcnt lgkmcnt(1)
	v_lshlrev_b32_e32 v154, 7, v153
	v_and_b32_e32 v154, 0x3f80, v154
	s_waitcnt lgkmcnt(0)
	v_and_b32_e32 v156, 0x7f, v155
	v_bitop3_b32 v162, v156, s9, v154 bitop3:0x36
	v_ashrrev_i32_e32 v154, 31, v155
	v_ashrrev_i32_e32 v156, 31, v153
	v_and_b32_e32 v154, 0x7fffffff, v154
	v_and_b32_e32 v156, 0x7fffffff, v156
	v_xor_b32_e32 v155, v154, v155
	v_xor_b32_e32 v154, v156, v153
	v_pk_add_f32 v[154:155], v[154:155], v[154:155] op_sel:[1,0] op_sel_hi:[0,1]
	ds_bpermute_b32 v153, v146, v159
	ds_bpermute_b32 v155, v147, v159
	v_and_or_b32 v154, v154, s10, v141
	v_cndmask_b32_e64 v163, v238, v154, s[4:5]
	ds_write2st64_b32 v142, v185, v186 offset1:1
	s_waitcnt lgkmcnt(2)
	v_lshlrev_b32_e32 v154, 7, v153
	v_and_b32_e32 v154, 0x3f80, v154
	s_waitcnt lgkmcnt(1)
	v_and_b32_e32 v156, 0x7f, v155
	v_bitop3_b32 v160, v156, s9, v154 bitop3:0x36
	v_ashrrev_i32_e32 v154, 31, v155
	v_ashrrev_i32_e32 v156, 31, v153
	v_and_b32_e32 v154, 0x7fffffff, v154
	v_and_b32_e32 v156, 0x7fffffff, v156
	v_xor_b32_e32 v155, v154, v155
	v_xor_b32_e32 v154, v156, v153
	ds_bpermute_b32 v153, v148, v159
	v_pk_add_f32 v[154:155], v[154:155], v[154:155] op_sel:[1,0] op_sel_hi:[0,1]
	ds_bpermute_b32 v155, v149, v159
	v_and_or_b32 v154, v154, s10, v141
	v_cndmask_b32_e64 v161, v238, v154, s[4:5]
	s_waitcnt lgkmcnt(1)
	v_lshlrev_b32_e32 v154, 7, v153
	v_and_b32_e32 v154, 0x3f80, v154
	s_waitcnt lgkmcnt(0)
	v_and_b32_e32 v156, 0x7f, v155
	v_bitop3_b32 v158, v156, s9, v154 bitop3:0x36
	v_ashrrev_i32_e32 v154, 31, v155
	v_ashrrev_i32_e32 v156, 31, v153
	v_and_b32_e32 v154, 0x7fffffff, v154
	v_and_b32_e32 v156, 0x7fffffff, v156
	v_xor_b32_e32 v155, v154, v155
	v_xor_b32_e32 v154, v156, v153
	ds_bpermute_b32 v153, v146, v167
	ds_bpermute_b32 v156, v147, v167
	v_pk_add_f32 v[154:155], v[154:155], v[154:155] op_sel:[1,0] op_sel_hi:[0,1]
	v_and_or_b32 v154, v154, s10, v141
	v_cndmask_b32_e64 v159, v238, v154, s[4:5]
	s_waitcnt lgkmcnt(1)
	v_lshlrev_b32_e32 v154, 7, v153
	v_and_b32_e32 v154, 0x3f80, v154
	s_waitcnt lgkmcnt(0)
	v_and_b32_e32 v155, 0x7f, v156
	v_bitop3_b32 v155, v155, s9, v154 bitop3:0x36
	v_ashrrev_i32_e32 v154, 31, v156
	v_ashrrev_i32_e32 v157, 31, v153
	ds_bpermute_b32 v167, v148, v167
	v_and_b32_e32 v154, 0x7fffffff, v154
	v_and_b32_e32 v168, 0x7fffffff, v157
	v_xor_b32_e32 v157, v154, v156
	v_xor_b32_e32 v156, v168, v153
	v_pk_add_f32 v[156:157], v[156:157], v[156:157] op_sel:[1,0] op_sel_hi:[0,1]
	v_and_or_b32 v153, v156, s10, v141
	v_cndmask_b32_e64 v157, v238, v153, s[4:5]
	v_ashrrev_i32_e32 v153, 31, v187
	s_waitcnt lgkmcnt(0)
	v_ashrrev_i32_e32 v154, 31, v167
	v_and_b32_e32 v153, 0x7fffffff, v153
	v_and_b32_e32 v154, 0x7fffffff, v154
	v_xor_b32_e32 v169, v153, v187
	v_xor_b32_e32 v168, v154, v167
	v_pk_add_f32 v[168:169], v[168:169], v[168:169] op_sel:[1,0] op_sel_hi:[0,1]
	v_and_or_b32 v153, v168, s10, v141
	v_cndmask_b32_e64 v153, v238, v153, s[4:5]
	ds_write2st64_b32 v142, v165, v163 offset0:2 offset1:3
	ds_write2st64_b32 v142, v161, v159 offset0:4 offset1:5
	ds_write2st64_b32 v142, v157, v153 offset0:6 offset1:7
	s_waitcnt lgkmcnt(0)
	v_mov_b32_e32 v154, s84
	ds_read_b128 v[168:171], v154
	v_lshlrev_b32_e32 v156, 7, v167
	ds_read_b128 v[172:175], v154 offset:16
	ds_read_b128 v[176:179], v154 offset:32
	ds_read_b128 v[180:183], v154 offset:48
	v_and_b32_e32 v156, 0x3f80, v156
	s_waitcnt lgkmcnt(3)
	v_cmp_gt_f32_e64 s[16:17], v169, v185
	v_cmp_gt_f32_e32 vcc, v168, v185
	v_cmp_gt_f32_e64 s[98:99], v170, v185
	v_cndmask_b32_e64 v167, 0, 1, s[16:17]
	v_addc_co_u32_e32 v167, vcc, 0, v167, vcc
	v_cmp_gt_f32_e32 vcc, v171, v185
	v_cndmask_b32_e64 v168, 0, 1, s[98:99]
	s_nop 0
	v_addc_co_u32_e32 v167, vcc, v167, v168, vcc
	s_waitcnt lgkmcnt(2)
	v_cmp_gt_f32_e64 s[16:17], v172, v185
	v_cmp_gt_f32_e32 vcc, v173, v185
	v_cmp_gt_f32_e64 s[98:99], v174, v185
	v_cndmask_b32_e64 v168, 0, 1, s[16:17]
	v_addc_co_u32_e32 v167, vcc, v167, v168, vcc
	v_cmp_gt_f32_e32 vcc, v175, v185
	v_cndmask_b32_e64 v168, 0, 1, s[98:99]
	s_nop 0
	v_addc_co_u32_e32 v167, vcc, v167, v168, vcc
	s_waitcnt lgkmcnt(1)
	v_cmp_gt_f32_e64 s[16:17], v176, v185
	v_cmp_gt_f32_e32 vcc, v177, v185
	v_cmp_gt_f32_e64 s[98:99], v178, v185
	v_cndmask_b32_e64 v168, 0, 1, s[16:17]
	v_addc_co_u32_e32 v167, vcc, v167, v168, vcc
	v_cmp_gt_f32_e32 vcc, v179, v185
	v_cndmask_b32_e64 v168, 0, 1, s[98:99]
	s_nop 0
	v_addc_co_u32_e32 v167, vcc, v167, v168, vcc
	s_waitcnt lgkmcnt(0)
	v_cmp_gt_f32_e64 s[16:17], v180, v185
	v_cmp_gt_f32_e32 vcc, v181, v185
	s_nop 0
	v_cndmask_b32_e64 v168, 0, 1, s[16:17]
	v_addc_co_u32_e32 v167, vcc, v167, v168, vcc
	ds_read_b128 v[168:171], v154 offset:64
	v_cmp_gt_f32_e64 s[16:17], v182, v185
	v_cmp_gt_f32_e32 vcc, v183, v185
	s_nop 0
	v_cndmask_b32_e64 v172, 0, 1, s[16:17]
	v_addc_co_u32_e32 v167, vcc, v167, v172, vcc
	ds_read_b128 v[172:175], v154 offset:80
	s_waitcnt lgkmcnt(1)
	v_cmp_gt_f32_e64 s[16:17], v168, v185
	v_cmp_gt_f32_e32 vcc, v169, v185
	v_cmp_gt_f32_e64 s[98:99], v170, v185
	v_cndmask_b32_e64 v168, 0, 1, s[16:17]
	v_addc_co_u32_e32 v167, vcc, v167, v168, vcc
	v_cmp_gt_f32_e32 vcc, v171, v185
	v_cndmask_b32_e64 v168, 0, 1, s[98:99]
	s_nop 0
	v_addc_co_u32_e32 v167, vcc, v167, v168, vcc
	s_waitcnt lgkmcnt(0)
	v_cmp_gt_f32_e64 s[16:17], v172, v185
	v_cmp_gt_f32_e32 vcc, v173, v185
	s_nop 0
	v_cndmask_b32_e64 v168, 0, 1, s[16:17]
	v_addc_co_u32_e32 v167, vcc, v167, v168, vcc
	ds_read_b128 v[168:171], v154 offset:96
	v_cmp_gt_f32_e64 s[16:17], v174, v185
	v_cmp_gt_f32_e32 vcc, v175, v185
	s_nop 0
	v_cndmask_b32_e64 v172, 0, 1, s[16:17]
	v_addc_co_u32_e32 v167, vcc, v167, v172, vcc
	ds_read_b128 v[172:175], v154 offset:112
	s_waitcnt lgkmcnt(1)
	v_cmp_gt_f32_e64 s[16:17], v168, v185
	v_cmp_gt_f32_e32 vcc, v169, v185
	v_cmp_gt_f32_e64 s[98:99], v170, v185
	v_cndmask_b32_e64 v168, 0, 1, s[16:17]
	v_addc_co_u32_e32 v167, vcc, v167, v168, vcc
	v_cmp_gt_f32_e32 vcc, v171, v185
	v_cndmask_b32_e64 v168, 0, 1, s[98:99]
	s_nop 0
	v_addc_co_u32_e32 v167, vcc, v167, v168, vcc
	s_waitcnt lgkmcnt(0)
	v_cmp_gt_f32_e64 s[16:17], v172, v185
	v_cmp_gt_f32_e32 vcc, v173, v185
	s_nop 0
	v_cndmask_b32_e64 v168, 0, 1, s[16:17]
	v_addc_co_u32_e32 v167, vcc, v167, v168, vcc
	ds_read_b128 v[168:171], v154 offset:128
	v_cmp_gt_f32_e64 s[16:17], v174, v185
	v_cmp_gt_f32_e32 vcc, v175, v185
	s_nop 0
	v_cndmask_b32_e64 v172, 0, 1, s[16:17]
	v_addc_co_u32_e32 v167, vcc, v167, v172, vcc
	ds_read_b128 v[172:175], v154 offset:144
	s_waitcnt lgkmcnt(1)
	v_cmp_gt_f32_e64 s[16:17], v168, v185
	v_cmp_gt_f32_e32 vcc, v169, v185
	v_cmp_gt_f32_e64 s[98:99], v170, v185
	v_cndmask_b32_e64 v168, 0, 1, s[16:17]
	v_addc_co_u32_e32 v167, vcc, v167, v168, vcc
	v_cmp_gt_f32_e32 vcc, v171, v185
	v_cndmask_b32_e64 v168, 0, 1, s[98:99]
	s_nop 0
	v_addc_co_u32_e32 v167, vcc, v167, v168, vcc
	s_waitcnt lgkmcnt(0)
	v_cmp_gt_f32_e64 s[16:17], v172, v185
	v_cmp_gt_f32_e32 vcc, v173, v185
	s_nop 0
	v_cndmask_b32_e64 v168, 0, 1, s[16:17]
	v_addc_co_u32_e32 v167, vcc, v167, v168, vcc
	ds_read_b128 v[168:171], v154 offset:160
	v_cmp_gt_f32_e64 s[16:17], v174, v185
	v_cmp_gt_f32_e32 vcc, v175, v185
	s_nop 0
	v_cndmask_b32_e64 v172, 0, 1, s[16:17]
	v_addc_co_u32_e32 v167, vcc, v167, v172, vcc
	ds_read_b128 v[172:175], v154 offset:176
	s_waitcnt lgkmcnt(1)
	v_cmp_gt_f32_e64 s[16:17], v168, v185
	v_cmp_gt_f32_e32 vcc, v169, v185
	v_cmp_gt_f32_e64 s[98:99], v170, v185
	v_cndmask_b32_e64 v168, 0, 1, s[16:17]
	v_addc_co_u32_e32 v167, vcc, v167, v168, vcc
	v_cmp_gt_f32_e32 vcc, v171, v185
	v_cndmask_b32_e64 v168, 0, 1, s[98:99]
	s_nop 0
	v_addc_co_u32_e32 v167, vcc, v167, v168, vcc
	s_waitcnt lgkmcnt(0)
	v_cmp_gt_f32_e64 s[16:17], v172, v185
	v_cmp_gt_f32_e32 vcc, v173, v185
	s_nop 0
	v_cndmask_b32_e64 v168, 0, 1, s[16:17]
	v_addc_co_u32_e32 v167, vcc, v167, v168, vcc
	ds_read_b128 v[168:171], v154 offset:192
	v_cmp_gt_f32_e64 s[16:17], v174, v185
	v_cmp_gt_f32_e32 vcc, v175, v185
	s_nop 0
	v_cndmask_b32_e64 v172, 0, 1, s[16:17]
	v_addc_co_u32_e32 v167, vcc, v167, v172, vcc
	ds_read_b128 v[172:175], v154 offset:256
	s_waitcnt lgkmcnt(1)
	v_cmp_gt_f32_e32 vcc, v168, v185
	s_nop 1
	v_cndmask_b32_e64 v168, 0, 1, vcc
	v_cmp_gt_f32_e32 vcc, v169, v185
	v_and_b32_e32 v169, 0x7f, v187
	v_bitop3_b32 v156, v169, s9, v156 bitop3:0x36
	v_addc_co_u32_e32 v167, vcc, v167, v168, vcc
	s_nop 0
	s_nop 0
	s_nop 0
	s_nop 0
	s_nop 0
	v_cmp_gt_u32_e32 vcc, 16, v167
	s_and_b64 vcc, s[4:5], vcc
	s_nop 0
	v_cndmask_b32_e32 v167, v150, v167, vcc
	v_lshlrev_b32_e32 v167, 2, v167
	ds_permute_b32 v168, v167, v185
	s_waitcnt lgkmcnt(1)
	v_cmp_gt_f32_e32 vcc, v173, v186
	ds_permute_b32 v176, v167, v184
	s_waitcnt lgkmcnt(1)
	v_cndmask_b32_e64 v177, 0, v168, s[44:45]
	v_cndmask_b32_e64 v167, 0, 1, vcc
	v_cmp_gt_f32_e32 vcc, v172, v186
	ds_read_b128 v[168:171], v154 offset:272
	s_nop 0
	v_addc_co_u32_e32 v167, vcc, 0, v167, vcc
	v_cmp_gt_f32_e64 s[16:17], v174, v186
	v_cmp_gt_f32_e32 vcc, v175, v186
	s_nop 0
	v_cndmask_b32_e64 v172, 0, 1, s[16:17]
	v_addc_co_u32_e32 v167, vcc, v167, v172, vcc
	ds_read_b128 v[172:175], v154 offset:288
	s_waitcnt lgkmcnt(1)
	v_cmp_gt_f32_e64 s[16:17], v168, v186
	v_cmp_gt_f32_e32 vcc, v169, v186
	v_cmp_gt_f32_e64 s[98:99], v170, v186
	v_cndmask_b32_e64 v168, 0, 1, s[16:17]
	v_addc_co_u32_e32 v167, vcc, v167, v168, vcc
	v_cmp_gt_f32_e32 vcc, v171, v186
	v_cndmask_b32_e64 v168, 0, 1, s[98:99]
	s_nop 0
	v_addc_co_u32_e32 v167, vcc, v167, v168, vcc
	s_waitcnt lgkmcnt(0)
	v_cmp_gt_f32_e64 s[16:17], v172, v186
	v_cmp_gt_f32_e32 vcc, v173, v186
	s_nop 0
	v_cndmask_b32_e64 v168, 0, 1, s[16:17]
	v_addc_co_u32_e32 v167, vcc, v167, v168, vcc
	ds_read_b128 v[168:171], v154 offset:304
	v_cmp_gt_f32_e64 s[16:17], v174, v186
	v_cmp_gt_f32_e32 vcc, v175, v186
	s_nop 0
	v_cndmask_b32_e64 v172, 0, 1, s[16:17]
	v_addc_co_u32_e32 v167, vcc, v167, v172, vcc
	ds_read_b128 v[172:175], v154 offset:320
	s_waitcnt lgkmcnt(1)
	v_cmp_gt_f32_e64 s[16:17], v168, v186
	v_cmp_gt_f32_e32 vcc, v169, v186
	v_cmp_gt_f32_e64 s[98:99], v170, v186
	v_cndmask_b32_e64 v168, 0, 1, s[16:17]
	v_addc_co_u32_e32 v167, vcc, v167, v168, vcc
	v_cmp_gt_f32_e32 vcc, v171, v186
	v_cndmask_b32_e64 v168, 0, 1, s[98:99]
	s_nop 0
	v_addc_co_u32_e32 v167, vcc, v167, v168, vcc
	s_waitcnt lgkmcnt(0)
	v_cmp_gt_f32_e64 s[16:17], v172, v186
	v_cmp_gt_f32_e32 vcc, v173, v186
	s_nop 0
	v_cndmask_b32_e64 v168, 0, 1, s[16:17]
	v_addc_co_u32_e32 v167, vcc, v167, v168, vcc
	ds_read_b128 v[168:171], v154 offset:336
	v_cmp_gt_f32_e64 s[16:17], v174, v186
	v_cmp_gt_f32_e32 vcc, v175, v186
	s_nop 0
	v_cndmask_b32_e64 v172, 0, 1, s[16:17]
	v_addc_co_u32_e32 v167, vcc, v167, v172, vcc
	ds_read_b128 v[172:175], v154 offset:352
	s_waitcnt lgkmcnt(1)
	v_cmp_gt_f32_e64 s[16:17], v168, v186
	v_cmp_gt_f32_e32 vcc, v169, v186
	v_cmp_gt_f32_e64 s[98:99], v170, v186
	v_cndmask_b32_e64 v168, 0, 1, s[16:17]
	v_addc_co_u32_e32 v167, vcc, v167, v168, vcc
	v_cmp_gt_f32_e32 vcc, v171, v186
	v_cndmask_b32_e64 v168, 0, 1, s[98:99]
	s_nop 0
	v_addc_co_u32_e32 v167, vcc, v167, v168, vcc
	s_waitcnt lgkmcnt(0)
	v_cmp_gt_f32_e64 s[16:17], v172, v186
	v_cmp_gt_f32_e32 vcc, v173, v186
	s_nop 0
	v_cndmask_b32_e64 v168, 0, 1, s[16:17]
	v_addc_co_u32_e32 v167, vcc, v167, v168, vcc
	ds_read_b128 v[168:171], v154 offset:368
	v_cmp_gt_f32_e64 s[16:17], v174, v186
	v_cmp_gt_f32_e32 vcc, v175, v186
	s_nop 0
	v_cndmask_b32_e64 v172, 0, 1, s[16:17]
	v_addc_co_u32_e32 v167, vcc, v167, v172, vcc
	ds_read_b128 v[172:175], v154 offset:384
	s_waitcnt lgkmcnt(1)
	v_cmp_gt_f32_e64 s[16:17], v168, v186
	v_cmp_gt_f32_e32 vcc, v169, v186
	v_cmp_gt_f32_e64 s[98:99], v170, v186
	v_cndmask_b32_e64 v168, 0, 1, s[16:17]
	v_addc_co_u32_e32 v167, vcc, v167, v168, vcc
	v_cmp_gt_f32_e32 vcc, v171, v186
	v_cndmask_b32_e64 v168, 0, 1, s[98:99]
	s_nop 0
	v_addc_co_u32_e32 v167, vcc, v167, v168, vcc
	s_waitcnt lgkmcnt(0)
	v_cmp_gt_f32_e64 s[16:17], v172, v186
	v_cmp_gt_f32_e32 vcc, v173, v186
	s_nop 0
	v_cndmask_b32_e64 v168, 0, 1, s[16:17]
	v_addc_co_u32_e32 v167, vcc, v167, v168, vcc
	ds_read_b128 v[168:171], v154 offset:400
	v_cmp_gt_f32_e64 s[16:17], v174, v186
	v_cmp_gt_f32_e32 vcc, v175, v186
	s_nop 0
	v_cndmask_b32_e64 v172, 0, 1, s[16:17]
	v_addc_co_u32_e32 v167, vcc, v167, v172, vcc
	ds_read_b128 v[172:175], v154 offset:416
	s_waitcnt lgkmcnt(1)
	v_cmp_gt_f32_e64 s[16:17], v168, v186
	v_cmp_gt_f32_e32 vcc, v169, v186
	v_cmp_gt_f32_e64 s[98:99], v170, v186
	v_cndmask_b32_e64 v168, 0, 1, s[16:17]
	v_addc_co_u32_e32 v167, vcc, v167, v168, vcc
	v_cmp_gt_f32_e32 vcc, v171, v186
	v_cndmask_b32_e64 v168, 0, 1, s[98:99]
	s_nop 0
	v_addc_co_u32_e32 v167, vcc, v167, v168, vcc
	s_waitcnt lgkmcnt(0)
	v_cmp_gt_f32_e64 s[16:17], v172, v186
	v_cmp_gt_f32_e32 vcc, v173, v186
	s_nop 0
	v_cndmask_b32_e64 v168, 0, 1, s[16:17]
	v_addc_co_u32_e32 v167, vcc, v167, v168, vcc
	ds_read_b128 v[168:171], v154 offset:432
	v_cmp_gt_f32_e64 s[16:17], v174, v186
	v_cmp_gt_f32_e32 vcc, v175, v186
	s_nop 0
	v_cndmask_b32_e64 v172, 0, 1, s[16:17]
	v_addc_co_u32_e32 v167, vcc, v167, v172, vcc
	ds_read_b128 v[172:175], v154 offset:448
	s_waitcnt lgkmcnt(1)
	v_cmp_gt_f32_e64 s[16:17], v168, v186
	v_cmp_gt_f32_e32 vcc, v169, v186
	v_cmp_gt_f32_e64 s[98:99], v170, v186
	v_cndmask_b32_e64 v168, 0, 1, s[16:17]
	v_addc_co_u32_e32 v167, vcc, v167, v168, vcc
	v_cmp_gt_f32_e32 vcc, v171, v186
	v_cndmask_b32_e64 v168, 0, 1, s[98:99]
	s_nop 0
	v_addc_co_u32_e32 v167, vcc, v167, v168, vcc
	s_waitcnt lgkmcnt(0)
	v_cmp_gt_f32_e64 s[16:17], v172, v186
	v_cmp_gt_f32_e32 vcc, v173, v186
	s_nop 0
	v_cndmask_b32_e64 v168, 0, 1, s[16:17]
	v_addc_co_u32_e32 v167, vcc, v167, v168, vcc
	s_nop 0
	s_nop 1
	s_nop 0
	s_nop 0
	ds_read_b128 v[172:175], v154 offset:528
	s_nop 0
	s_nop 0
	ds_read_b128 v[168:171], v154 offset:512
	v_cmp_gt_u32_e32 vcc, 16, v167
	v_add_u32_e32 v167, 16, v167
	s_and_b64 vcc, s[4:5], vcc
	v_cndmask_b32_e32 v167, v151, v167, vcc
	v_lshlrev_b32_e32 v167, 2, v167
	s_waitcnt lgkmcnt(0)
	v_cmp_gt_f32_e32 vcc, v169, v165
	ds_permute_b32 v179, v167, v166
	ds_permute_b32 v178, v167, v186
	v_cndmask_b32_e64 v166, 0, 1, vcc
	v_cmp_gt_f32_e32 vcc, v168, v165
	s_nop 1
	v_addc_co_u32_e32 v166, vcc, 0, v166, vcc
	v_cmp_gt_f32_e64 s[16:17], v170, v165
	v_cmp_gt_f32_e32 vcc, v171, v165
	v_cmp_gt_f32_e64 s[98:99], v172, v165
	v_cndmask_b32_e64 v167, 0, 1, s[16:17]
	v_addc_co_u32_e32 v166, vcc, v166, v167, vcc
	v_cmp_gt_f32_e32 vcc, v173, v165
	v_cndmask_b32_e64 v167, 0, 1, s[98:99]
	s_nop 0
	v_addc_co_u32_e32 v170, vcc, v166, v167, vcc
	ds_read_b128 v[166:169], v154 offset:544
	v_cmp_gt_f32_e64 s[16:17], v174, v165
	v_cmp_gt_f32_e32 vcc, v175, v165
	s_nop 0
	v_cndmask_b32_e64 v171, 0, 1, s[16:17]
	v_addc_co_u32_e32 v174, vcc, v170, v171, vcc
	ds_read_b128 v[170:173], v154 offset:560
	s_waitcnt lgkmcnt(1)
	v_cmp_gt_f32_e64 s[16:17], v166, v165
	v_cmp_gt_f32_e32 vcc, v167, v165
	v_cmp_gt_f32_e64 s[98:99], v168, v165
	v_cndmask_b32_e64 v166, 0, 1, s[16:17]
	v_addc_co_u32_e32 v166, vcc, v174, v166, vcc
	v_cmp_gt_f32_e32 vcc, v169, v165
	v_cndmask_b32_e64 v167, 0, 1, s[98:99]
	s_nop 0
	v_addc_co_u32_e32 v166, vcc, v166, v167, vcc
	s_waitcnt lgkmcnt(0)
	v_cmp_gt_f32_e64 s[16:17], v170, v165
	v_cmp_gt_f32_e32 vcc, v171, v165
	s_nop 0
	v_cndmask_b32_e64 v167, 0, 1, s[16:17]
	v_addc_co_u32_e32 v170, vcc, v166, v167, vcc
	ds_read_b128 v[166:169], v154 offset:576
	v_cmp_gt_f32_e64 s[16:17], v172, v165
	v_cmp_gt_f32_e32 vcc, v173, v165
	s_nop 0
	v_cndmask_b32_e64 v171, 0, 1, s[16:17]
	v_addc_co_u32_e32 v174, vcc, v170, v171, vcc
	ds_read_b128 v[170:173], v154 offset:592
	s_waitcnt lgkmcnt(1)
	v_cmp_gt_f32_e64 s[16:17], v166, v165
	v_cmp_gt_f32_e32 vcc, v167, v165
	v_cmp_gt_f32_e64 s[98:99], v168, v165
	v_cndmask_b32_e64 v166, 0, 1, s[16:17]
	v_addc_co_u32_e32 v166, vcc, v174, v166, vcc
	v_cmp_gt_f32_e32 vcc, v169, v165
	v_cndmask_b32_e64 v167, 0, 1, s[98:99]
	s_nop 0
	v_addc_co_u32_e32 v166, vcc, v166, v167, vcc
	s_waitcnt lgkmcnt(0)
	v_cmp_gt_f32_e64 s[16:17], v170, v165
	v_cmp_gt_f32_e32 vcc, v171, v165
	s_nop 0
	v_cndmask_b32_e64 v167, 0, 1, s[16:17]
	v_addc_co_u32_e32 v170, vcc, v166, v167, vcc
	ds_read_b128 v[166:169], v154 offset:608
	v_cmp_gt_f32_e64 s[16:17], v172, v165
	v_cmp_gt_f32_e32 vcc, v173, v165
	s_nop 0
	v_cndmask_b32_e64 v171, 0, 1, s[16:17]
	v_addc_co_u32_e32 v174, vcc, v170, v171, vcc
	ds_read_b128 v[170:173], v154 offset:624
	s_waitcnt lgkmcnt(1)
	v_cmp_gt_f32_e64 s[16:17], v166, v165
	v_cmp_gt_f32_e32 vcc, v167, v165
	v_cmp_gt_f32_e64 s[98:99], v168, v165
	v_cndmask_b32_e64 v166, 0, 1, s[16:17]
	v_addc_co_u32_e32 v166, vcc, v174, v166, vcc
	v_cmp_gt_f32_e32 vcc, v169, v165
	v_cndmask_b32_e64 v167, 0, 1, s[98:99]
	s_nop 0
	v_addc_co_u32_e32 v166, vcc, v166, v167, vcc
	s_waitcnt lgkmcnt(0)
	v_cmp_gt_f32_e64 s[16:17], v170, v165
	v_cmp_gt_f32_e32 vcc, v171, v165
	s_nop 0
	v_cndmask_b32_e64 v167, 0, 1, s[16:17]
	v_addc_co_u32_e32 v170, vcc, v166, v167, vcc
	ds_read_b128 v[166:169], v154 offset:640
	v_cmp_gt_f32_e64 s[16:17], v172, v165
	v_cmp_gt_f32_e32 vcc, v173, v165
	s_nop 0
	v_cndmask_b32_e64 v171, 0, 1, s[16:17]
	v_addc_co_u32_e32 v174, vcc, v170, v171, vcc
	ds_read_b128 v[170:173], v154 offset:656
	s_waitcnt lgkmcnt(1)
	v_cmp_gt_f32_e64 s[16:17], v166, v165
	v_cmp_gt_f32_e32 vcc, v167, v165
	v_cmp_gt_f32_e64 s[98:99], v168, v165
	v_cndmask_b32_e64 v166, 0, 1, s[16:17]
	v_addc_co_u32_e32 v166, vcc, v174, v166, vcc
	v_cmp_gt_f32_e32 vcc, v169, v165
	v_cndmask_b32_e64 v167, 0, 1, s[98:99]
	s_nop 0
	v_addc_co_u32_e32 v166, vcc, v166, v167, vcc
	s_waitcnt lgkmcnt(0)
	v_cmp_gt_f32_e64 s[16:17], v170, v165
	v_cmp_gt_f32_e32 vcc, v171, v165
	s_nop 0
	v_cndmask_b32_e64 v167, 0, 1, s[16:17]
	v_addc_co_u32_e32 v170, vcc, v166, v167, vcc
	ds_read_b128 v[166:169], v154 offset:672
	v_cmp_gt_f32_e64 s[16:17], v172, v165
	v_cmp_gt_f32_e32 vcc, v173, v165
	s_nop 0
	v_cndmask_b32_e64 v171, 0, 1, s[16:17]
	v_addc_co_u32_e32 v174, vcc, v170, v171, vcc
	ds_read_b128 v[170:173], v154 offset:688
	s_waitcnt lgkmcnt(1)
	v_cmp_gt_f32_e64 s[16:17], v166, v165
	v_cmp_gt_f32_e32 vcc, v167, v165
	v_cmp_gt_f32_e64 s[98:99], v168, v165
	v_cndmask_b32_e64 v166, 0, 1, s[16:17]
	v_addc_co_u32_e32 v166, vcc, v174, v166, vcc
	v_cmp_gt_f32_e32 vcc, v169, v165
	v_cndmask_b32_e64 v167, 0, 1, s[98:99]
	s_nop 0
	v_addc_co_u32_e32 v166, vcc, v166, v167, vcc
	s_waitcnt lgkmcnt(0)
	v_cmp_gt_f32_e64 s[16:17], v170, v165
	v_cmp_gt_f32_e32 vcc, v171, v165
	s_nop 0
	v_cndmask_b32_e64 v167, 0, 1, s[16:17]
	v_addc_co_u32_e32 v170, vcc, v166, v167, vcc
	ds_read_b128 v[166:169], v154 offset:704
	v_cmp_gt_f32_e64 s[16:17], v172, v165
	v_cmp_gt_f32_e32 vcc, v173, v165
	s_nop 0
	v_cndmask_b32_e64 v171, 0, 1, s[16:17]
	v_addc_co_u32_e32 v174, vcc, v170, v171, vcc
	ds_read_b128 v[170:173], v154 offset:768
	s_waitcnt lgkmcnt(1)
	v_cmp_gt_f32_e64 s[16:17], v166, v165
	v_cmp_gt_f32_e32 vcc, v167, v165
	s_nop 0
	v_cndmask_b32_e64 v166, 0, 1, s[16:17]
	v_addc_co_u32_e32 v166, vcc, v174, v166, vcc
	s_nop 0
	v_cndmask_b32_e64 v168, v177, v178, s[46:47]
	s_nop 0
	s_nop 0
	s_nop 0
	s_nop 1
	s_nop 0
	v_cmp_gt_u32_e32 vcc, 16, v166
	v_add_u32_e32 v166, 32, v166
	s_and_b64 vcc, s[4:5], vcc
	v_cndmask_b32_e32 v166, v152, v166, vcc
	v_lshlrev_b32_e32 v166, 2, v166
	ds_permute_b32 v165, v166, v165
	s_waitcnt lgkmcnt(1)
	v_cmp_gt_f32_e32 vcc, v171, v163
	v_cndmask_b32_e64 v167, 0, v176, s[44:45]
	ds_permute_b32 v175, v166, v164
	v_cndmask_b32_e64 v164, 0, 1, vcc
	v_cmp_gt_f32_e32 vcc, v170, v163
	v_cndmask_b32_e64 v174, v167, v179, s[46:47]
	s_waitcnt lgkmcnt(1)
	v_cndmask_b32_e64 v176, v168, v165, s[48:49]
	v_addc_co_u32_e32 v168, vcc, 0, v164, vcc
	ds_read_b128 v[164:167], v154 offset:784
	v_cmp_gt_f32_e64 s[16:17], v172, v163
	v_cmp_gt_f32_e32 vcc, v173, v163
	s_nop 0
	v_cndmask_b32_e64 v169, 0, 1, s[16:17]
	v_addc_co_u32_e32 v172, vcc, v168, v169, vcc
	ds_read_b128 v[168:171], v154 offset:800
	s_waitcnt lgkmcnt(1)
	v_cmp_gt_f32_e64 s[16:17], v164, v163
	v_cmp_gt_f32_e32 vcc, v165, v163
	v_cmp_gt_f32_e64 s[98:99], v166, v163
	v_cndmask_b32_e64 v164, 0, 1, s[16:17]
	v_addc_co_u32_e32 v164, vcc, v172, v164, vcc
	v_cmp_gt_f32_e32 vcc, v167, v163
	v_cndmask_b32_e64 v165, 0, 1, s[98:99]
	s_nop 0
	v_addc_co_u32_e32 v164, vcc, v164, v165, vcc
	s_waitcnt lgkmcnt(0)
	v_cmp_gt_f32_e64 s[16:17], v168, v163
	v_cmp_gt_f32_e32 vcc, v169, v163
	s_nop 0
	v_cndmask_b32_e64 v165, 0, 1, s[16:17]
	v_addc_co_u32_e32 v168, vcc, v164, v165, vcc
	ds_read_b128 v[164:167], v154 offset:816
	v_cmp_gt_f32_e64 s[16:17], v170, v163
	v_cmp_gt_f32_e32 vcc, v171, v163
	s_nop 0
	v_cndmask_b32_e64 v169, 0, 1, s[16:17]
	v_addc_co_u32_e32 v172, vcc, v168, v169, vcc
	ds_read_b128 v[168:171], v154 offset:832
	s_waitcnt lgkmcnt(1)
	v_cmp_gt_f32_e64 s[16:17], v164, v163
	v_cmp_gt_f32_e32 vcc, v165, v163
	v_cmp_gt_f32_e64 s[98:99], v166, v163
	v_cndmask_b32_e64 v164, 0, 1, s[16:17]
	v_addc_co_u32_e32 v164, vcc, v172, v164, vcc
	v_cmp_gt_f32_e32 vcc, v167, v163
	v_cndmask_b32_e64 v165, 0, 1, s[98:99]
	s_nop 0
	v_addc_co_u32_e32 v164, vcc, v164, v165, vcc
	s_waitcnt lgkmcnt(0)
	v_cmp_gt_f32_e64 s[16:17], v168, v163
	v_cmp_gt_f32_e32 vcc, v169, v163
	s_nop 0
	v_cndmask_b32_e64 v165, 0, 1, s[16:17]
	v_addc_co_u32_e32 v168, vcc, v164, v165, vcc
	ds_read_b128 v[164:167], v154 offset:848
	v_cmp_gt_f32_e64 s[16:17], v170, v163
	v_cmp_gt_f32_e32 vcc, v171, v163
	s_nop 0
	v_cndmask_b32_e64 v169, 0, 1, s[16:17]
	v_addc_co_u32_e32 v172, vcc, v168, v169, vcc
	ds_read_b128 v[168:171], v154 offset:864
	s_waitcnt lgkmcnt(1)
	v_cmp_gt_f32_e64 s[16:17], v164, v163
	v_cmp_gt_f32_e32 vcc, v165, v163
	v_cmp_gt_f32_e64 s[98:99], v166, v163
	v_cndmask_b32_e64 v164, 0, 1, s[16:17]
	v_addc_co_u32_e32 v164, vcc, v172, v164, vcc
	v_cmp_gt_f32_e32 vcc, v167, v163
	v_cndmask_b32_e64 v165, 0, 1, s[98:99]
	s_nop 0
	v_addc_co_u32_e32 v164, vcc, v164, v165, vcc
	s_waitcnt lgkmcnt(0)
	v_cmp_gt_f32_e64 s[16:17], v168, v163
	v_cmp_gt_f32_e32 vcc, v169, v163
	s_nop 0
	v_cndmask_b32_e64 v165, 0, 1, s[16:17]
	v_addc_co_u32_e32 v168, vcc, v164, v165, vcc
	ds_read_b128 v[164:167], v154 offset:880
	v_cmp_gt_f32_e64 s[16:17], v170, v163
	v_cmp_gt_f32_e32 vcc, v171, v163
	s_nop 0
	v_cndmask_b32_e64 v169, 0, 1, s[16:17]
	v_addc_co_u32_e32 v172, vcc, v168, v169, vcc
	ds_read_b128 v[168:171], v154 offset:896
	s_waitcnt lgkmcnt(1)
	v_cmp_gt_f32_e64 s[16:17], v164, v163
	v_cmp_gt_f32_e32 vcc, v165, v163
	v_cmp_gt_f32_e64 s[98:99], v166, v163
	v_cndmask_b32_e64 v164, 0, 1, s[16:17]
	v_addc_co_u32_e32 v164, vcc, v172, v164, vcc
	v_cmp_gt_f32_e32 vcc, v167, v163
	v_cndmask_b32_e64 v165, 0, 1, s[98:99]
	s_nop 0
	v_addc_co_u32_e32 v164, vcc, v164, v165, vcc
	s_waitcnt lgkmcnt(0)
	v_cmp_gt_f32_e64 s[16:17], v168, v163
	v_cmp_gt_f32_e32 vcc, v169, v163
	s_nop 0
	v_cndmask_b32_e64 v165, 0, 1, s[16:17]
	v_addc_co_u32_e32 v168, vcc, v164, v165, vcc
	ds_read_b128 v[164:167], v154 offset:912
	v_cmp_gt_f32_e64 s[16:17], v170, v163
	v_cmp_gt_f32_e32 vcc, v171, v163
	s_nop 0
	v_cndmask_b32_e64 v169, 0, 1, s[16:17]
	v_addc_co_u32_e32 v172, vcc, v168, v169, vcc
	ds_read_b128 v[168:171], v154 offset:928
	s_waitcnt lgkmcnt(1)
	v_cmp_gt_f32_e64 s[16:17], v164, v163
	v_cmp_gt_f32_e32 vcc, v165, v163
	v_cmp_gt_f32_e64 s[98:99], v166, v163
	v_cndmask_b32_e64 v164, 0, 1, s[16:17]
	v_addc_co_u32_e32 v164, vcc, v172, v164, vcc
	v_cmp_gt_f32_e32 vcc, v167, v163
	v_cndmask_b32_e64 v165, 0, 1, s[98:99]
	s_nop 0
	v_addc_co_u32_e32 v164, vcc, v164, v165, vcc
	s_waitcnt lgkmcnt(0)
	v_cmp_gt_f32_e64 s[16:17], v168, v163
	v_cmp_gt_f32_e32 vcc, v169, v163
	s_nop 0
	v_cndmask_b32_e64 v165, 0, 1, s[16:17]
	v_addc_co_u32_e32 v168, vcc, v164, v165, vcc
	ds_read_b128 v[164:167], v154 offset:944
	v_cmp_gt_f32_e64 s[16:17], v170, v163
	v_cmp_gt_f32_e32 vcc, v171, v163
	s_nop 0
	v_cndmask_b32_e64 v169, 0, 1, s[16:17]
	v_addc_co_u32_e32 v172, vcc, v168, v169, vcc
	ds_read_b128 v[168:171], v154 offset:960
	s_waitcnt lgkmcnt(1)
	v_cmp_gt_f32_e64 s[16:17], v164, v163
	v_cmp_gt_f32_e32 vcc, v165, v163
	v_cmp_gt_f32_e64 s[98:99], v166, v163
	v_cndmask_b32_e64 v164, 0, 1, s[16:17]
	v_addc_co_u32_e32 v164, vcc, v172, v164, vcc
	v_cmp_gt_f32_e32 vcc, v167, v163
	v_cndmask_b32_e64 v165, 0, 1, s[98:99]
	s_nop 0
	v_addc_co_u32_e32 v164, vcc, v164, v165, vcc
	s_waitcnt lgkmcnt(0)
	v_cmp_gt_f32_e64 s[16:17], v168, v163
	v_cmp_gt_f32_e32 vcc, v169, v163
	s_nop 0
	v_cndmask_b32_e64 v165, 0, 1, s[16:17]
	v_addc_co_u32_e32 v164, vcc, v164, v165, vcc
	s_nop 0
	s_nop 0
	s_nop 0
	s_nop 0
	v_cmp_gt_u32_e32 vcc, 16, v164
	v_add_u32_e32 v164, 48, v164
	s_and_b64 vcc, s[4:5], vcc
	v_cndmask_b32_e32 v168, v140, v164, vcc
	ds_read_b128 v[164:167], v154 offset:1024
	v_lshlrev_b32_e32 v168, 2, v168
	ds_permute_b32 v172, v168, v163
	ds_permute_b32 v173, v168, v162
	ds_read_b128 v[168:171], v154 offset:1040
	s_waitcnt lgkmcnt(3)
	v_cmp_gt_f32_e64 s[16:17], v165, v161
	v_cmp_gt_f32_e32 vcc, v164, v161
	v_cmp_gt_f32_e64 s[98:99], v166, v161
	v_cndmask_b32_e64 v162, 0, 1, s[16:17]
	v_addc_co_u32_e32 v162, vcc, 0, v162, vcc
	v_cmp_gt_f32_e32 vcc, v167, v161
	v_cndmask_b32_e64 v163, 0, 1, s[98:99]
	s_nop 0
	v_addc_co_u32_e32 v162, vcc, v162, v163, vcc
	s_waitcnt lgkmcnt(0)
	v_cmp_gt_f32_e64 s[16:17], v168, v161
	v_cmp_gt_f32_e32 vcc, v169, v161
	s_nop 0
	v_cndmask_b32_e64 v163, 0, 1, s[16:17]
	v_addc_co_u32_e32 v166, vcc, v162, v163, vcc
	ds_read_b128 v[162:165], v154 offset:1056
	v_cmp_gt_f32_e64 s[16:17], v170, v161
	v_cmp_gt_f32_e32 vcc, v171, v161
	s_nop 0
	v_cndmask_b32_e64 v167, 0, 1, s[16:17]
	v_addc_co_u32_e32 v170, vcc, v166, v167, vcc
	ds_read_b128 v[166:169], v154 offset:1072
	s_waitcnt lgkmcnt(1)
	v_cmp_gt_f32_e64 s[16:17], v162, v161
	v_cmp_gt_f32_e32 vcc, v163, v161
	v_cmp_gt_f32_e64 s[98:99], v164, v161
	v_cndmask_b32_e64 v162, 0, 1, s[16:17]
	v_addc_co_u32_e32 v162, vcc, v170, v162, vcc
	v_cmp_gt_f32_e32 vcc, v165, v161
	v_cndmask_b32_e64 v163, 0, 1, s[98:99]
	s_nop 0
	v_addc_co_u32_e32 v162, vcc, v162, v163, vcc
	s_waitcnt lgkmcnt(0)
	v_cmp_gt_f32_e64 s[16:17], v166, v161
	v_cmp_gt_f32_e32 vcc, v167, v161
	s_nop 0
	v_cndmask_b32_e64 v163, 0, 1, s[16:17]
	v_addc_co_u32_e32 v166, vcc, v162, v163, vcc
	ds_read_b128 v[162:165], v154 offset:1088
	v_cmp_gt_f32_e64 s[16:17], v168, v161
	v_cmp_gt_f32_e32 vcc, v169, v161
	s_nop 0
	v_cndmask_b32_e64 v167, 0, 1, s[16:17]
	v_addc_co_u32_e32 v170, vcc, v166, v167, vcc
	ds_read_b128 v[166:169], v154 offset:1104
	s_waitcnt lgkmcnt(1)
	v_cmp_gt_f32_e64 s[16:17], v162, v161
	v_cmp_gt_f32_e32 vcc, v163, v161
	v_cmp_gt_f32_e64 s[98:99], v164, v161
	v_cndmask_b32_e64 v162, 0, 1, s[16:17]
	v_addc_co_u32_e32 v162, vcc, v170, v162, vcc
	v_cmp_gt_f32_e32 vcc, v165, v161
	v_cndmask_b32_e64 v163, 0, 1, s[98:99]
	s_nop 0
	v_addc_co_u32_e32 v162, vcc, v162, v163, vcc
	s_waitcnt lgkmcnt(0)
	v_cmp_gt_f32_e64 s[16:17], v166, v161
	v_cmp_gt_f32_e32 vcc, v167, v161
	s_nop 0
	v_cndmask_b32_e64 v163, 0, 1, s[16:17]
	v_addc_co_u32_e32 v166, vcc, v162, v163, vcc
	ds_read_b128 v[162:165], v154 offset:1120
	v_cmp_gt_f32_e64 s[16:17], v168, v161
	v_cmp_gt_f32_e32 vcc, v169, v161
	s_nop 0
	v_cndmask_b32_e64 v167, 0, 1, s[16:17]
	v_addc_co_u32_e32 v170, vcc, v166, v167, vcc
	ds_read_b128 v[166:169], v154 offset:1136
	s_waitcnt lgkmcnt(1)
	v_cmp_gt_f32_e64 s[16:17], v162, v161
	v_cmp_gt_f32_e32 vcc, v163, v161
	v_cmp_gt_f32_e64 s[98:99], v164, v161
	v_cndmask_b32_e64 v162, 0, 1, s[16:17]
	v_addc_co_u32_e32 v162, vcc, v170, v162, vcc
	v_cmp_gt_f32_e32 vcc, v165, v161
	v_cndmask_b32_e64 v163, 0, 1, s[98:99]
	s_nop 0
	v_addc_co_u32_e32 v162, vcc, v162, v163, vcc
	s_waitcnt lgkmcnt(0)
	v_cmp_gt_f32_e64 s[16:17], v166, v161
	v_cmp_gt_f32_e32 vcc, v167, v161
	s_nop 0
	v_cndmask_b32_e64 v163, 0, 1, s[16:17]
	v_addc_co_u32_e32 v166, vcc, v162, v163, vcc
	ds_read_b128 v[162:165], v154 offset:1152
	v_cmp_gt_f32_e64 s[16:17], v168, v161
	v_cmp_gt_f32_e32 vcc, v169, v161
	s_nop 0
	v_cndmask_b32_e64 v167, 0, 1, s[16:17]
	v_addc_co_u32_e32 v170, vcc, v166, v167, vcc
	ds_read_b128 v[166:169], v154 offset:1168
	s_waitcnt lgkmcnt(1)
	v_cmp_gt_f32_e64 s[16:17], v162, v161
	v_cmp_gt_f32_e32 vcc, v163, v161
	v_cmp_gt_f32_e64 s[98:99], v164, v161
	v_cndmask_b32_e64 v162, 0, 1, s[16:17]
	v_addc_co_u32_e32 v162, vcc, v170, v162, vcc
	v_cmp_gt_f32_e32 vcc, v165, v161
	v_cndmask_b32_e64 v163, 0, 1, s[98:99]
	s_nop 0
	v_addc_co_u32_e32 v162, vcc, v162, v163, vcc
	s_waitcnt lgkmcnt(0)
	v_cmp_gt_f32_e64 s[16:17], v166, v161
	v_cmp_gt_f32_e32 vcc, v167, v161
	s_nop 0
	v_cndmask_b32_e64 v163, 0, 1, s[16:17]
	v_addc_co_u32_e32 v166, vcc, v162, v163, vcc
	ds_read_b128 v[162:165], v154 offset:1184
	v_cmp_gt_f32_e64 s[16:17], v168, v161
	v_cmp_gt_f32_e32 vcc, v169, v161
	s_nop 0
	v_cndmask_b32_e64 v167, 0, 1, s[16:17]
	v_addc_co_u32_e32 v170, vcc, v166, v167, vcc
	ds_read_b128 v[166:169], v154 offset:1200
	s_waitcnt lgkmcnt(1)
	v_cmp_gt_f32_e64 s[16:17], v162, v161
	v_cmp_gt_f32_e32 vcc, v163, v161
	v_cmp_gt_f32_e64 s[98:99], v164, v161
	v_cndmask_b32_e64 v162, 0, 1, s[16:17]
	v_addc_co_u32_e32 v162, vcc, v170, v162, vcc
	v_cmp_gt_f32_e32 vcc, v165, v161
	v_cndmask_b32_e64 v163, 0, 1, s[98:99]
	s_nop 0
	v_addc_co_u32_e32 v162, vcc, v162, v163, vcc
	s_waitcnt lgkmcnt(0)
	v_cmp_gt_f32_e64 s[16:17], v166, v161
	v_cmp_gt_f32_e32 vcc, v167, v161
	s_nop 0
	v_cndmask_b32_e64 v163, 0, 1, s[16:17]
	v_addc_co_u32_e32 v166, vcc, v162, v163, vcc
	ds_read_b128 v[162:165], v154 offset:1216
	v_cmp_gt_f32_e64 s[16:17], v168, v161
	v_cmp_gt_f32_e32 vcc, v169, v161
	s_nop 0
	v_cndmask_b32_e64 v167, 0, 1, s[16:17]
	v_addc_co_u32_e32 v170, vcc, v166, v167, vcc
	ds_read_b128 v[166:169], v154 offset:1280
	s_waitcnt lgkmcnt(1)
	v_cmp_gt_f32_e64 s[16:17], v162, v161
	v_cmp_gt_f32_e32 vcc, v163, v161
	s_nop 0
	v_cndmask_b32_e64 v162, 0, 1, s[16:17]
	v_addc_co_u32_e32 v162, vcc, v170, v162, vcc
	s_nop 0
	s_nop 0
	s_nop 0
	s_nop 0
	v_cmp_gt_u32_e32 vcc, 16, v162
	s_and_b64 vcc, s[4:5], vcc
	s_nop 0
	v_cndmask_b32_e32 v162, v150, v162, vcc
	v_lshlrev_b32_e32 v163, 2, v162
	ds_permute_b32 v164, v163, v161
	s_waitcnt lgkmcnt(1)
	v_cmp_gt_f32_e32 vcc, v167, v159
	ds_permute_b32 v160, v163, v160
	v_cndmask_b32_e64 v162, v176, v172, s[50:51]
	v_cndmask_b32_e64 v161, v174, v175, s[48:49]
	s_waitcnt lgkmcnt(1)
	v_cndmask_b32_e64 v163, 0, v164, s[44:45]
	v_cndmask_b32_e64 v164, 0, 1, vcc
	v_cmp_gt_f32_e32 vcc, v166, v159
	s_waitcnt lgkmcnt(0)
	v_cndmask_b32_e64 v160, 0, v160, s[44:45]
	v_cndmask_b32_e64 v161, v161, v173, s[50:51]
	v_addc_co_u32_e32 v170, vcc, 0, v164, vcc
	ds_read_b128 v[164:167], v154 offset:1296
	v_cmp_gt_f32_e32 vcc, v168, v159
	v_lshlrev_b32_e32 v161, 7, v161
	s_nop 0
	v_cndmask_b32_e64 v168, 0, 1, vcc
	v_cmp_gt_f32_e32 vcc, v169, v159
	s_nop 1
	v_addc_co_u32_e32 v172, vcc, v170, v168, vcc
	ds_read_b128 v[168:171], v154 offset:1312
	s_waitcnt lgkmcnt(1)
	v_cmp_gt_f32_e64 s[16:17], v164, v159
	v_cmp_gt_f32_e32 vcc, v165, v159
	v_cmp_gt_f32_e64 s[98:99], v166, v159
	v_cndmask_b32_e64 v164, 0, 1, s[16:17]
	v_addc_co_u32_e32 v164, vcc, v172, v164, vcc
	v_cmp_gt_f32_e32 vcc, v167, v159
	v_cndmask_b32_e64 v165, 0, 1, s[98:99]
	s_nop 0
	v_addc_co_u32_e32 v164, vcc, v164, v165, vcc
	s_waitcnt lgkmcnt(0)
	v_cmp_gt_f32_e64 s[16:17], v168, v159
	v_cmp_gt_f32_e32 vcc, v169, v159
	s_nop 0
	v_cndmask_b32_e64 v165, 0, 1, s[16:17]
	v_addc_co_u32_e32 v168, vcc, v164, v165, vcc
	ds_read_b128 v[164:167], v154 offset:1328
	v_cmp_gt_f32_e64 s[16:17], v170, v159
	v_cmp_gt_f32_e32 vcc, v171, v159
	s_nop 0
	v_cndmask_b32_e64 v169, 0, 1, s[16:17]
	v_addc_co_u32_e32 v172, vcc, v168, v169, vcc
	ds_read_b128 v[168:171], v154 offset:1344
	s_waitcnt lgkmcnt(1)
	v_cmp_gt_f32_e64 s[16:17], v164, v159
	v_cmp_gt_f32_e32 vcc, v165, v159
	v_cmp_gt_f32_e64 s[98:99], v166, v159
	v_cndmask_b32_e64 v164, 0, 1, s[16:17]
	v_addc_co_u32_e32 v164, vcc, v172, v164, vcc
	v_cmp_gt_f32_e32 vcc, v167, v159
	v_cndmask_b32_e64 v165, 0, 1, s[98:99]
	s_nop 0
	v_addc_co_u32_e32 v164, vcc, v164, v165, vcc
	s_waitcnt lgkmcnt(0)
	v_cmp_gt_f32_e64 s[16:17], v168, v159
	v_cmp_gt_f32_e32 vcc, v169, v159
	s_nop 0
	v_cndmask_b32_e64 v165, 0, 1, s[16:17]
	v_addc_co_u32_e32 v168, vcc, v164, v165, vcc
	ds_read_b128 v[164:167], v154 offset:1360
	v_cmp_gt_f32_e64 s[16:17], v170, v159
	v_cmp_gt_f32_e32 vcc, v171, v159
	s_nop 0
	v_cndmask_b32_e64 v169, 0, 1, s[16:17]
	v_addc_co_u32_e32 v172, vcc, v168, v169, vcc
	ds_read_b128 v[168:171], v154 offset:1376
	s_waitcnt lgkmcnt(1)
	v_cmp_gt_f32_e64 s[16:17], v164, v159
	v_cmp_gt_f32_e32 vcc, v165, v159
	v_cmp_gt_f32_e64 s[98:99], v166, v159
	v_cndmask_b32_e64 v164, 0, 1, s[16:17]
	v_addc_co_u32_e32 v164, vcc, v172, v164, vcc
	v_cmp_gt_f32_e32 vcc, v167, v159
	v_cndmask_b32_e64 v165, 0, 1, s[98:99]
	s_nop 0
	v_addc_co_u32_e32 v164, vcc, v164, v165, vcc
	s_waitcnt lgkmcnt(0)
	v_cmp_gt_f32_e64 s[16:17], v168, v159
	v_cmp_gt_f32_e32 vcc, v169, v159
	s_nop 0
	v_cndmask_b32_e64 v165, 0, 1, s[16:17]
	v_addc_co_u32_e32 v168, vcc, v164, v165, vcc
	ds_read_b128 v[164:167], v154 offset:1392
	v_cmp_gt_f32_e64 s[16:17], v170, v159
	v_cmp_gt_f32_e32 vcc, v171, v159
	s_nop 0
	v_cndmask_b32_e64 v169, 0, 1, s[16:17]
	v_addc_co_u32_e32 v172, vcc, v168, v169, vcc
	ds_read_b128 v[168:171], v154 offset:1408
	s_waitcnt lgkmcnt(1)
	v_cmp_gt_f32_e64 s[16:17], v164, v159
	v_cmp_gt_f32_e32 vcc, v165, v159
	v_cmp_gt_f32_e64 s[98:99], v166, v159
	v_cndmask_b32_e64 v164, 0, 1, s[16:17]
	v_addc_co_u32_e32 v164, vcc, v172, v164, vcc
	v_cmp_gt_f32_e32 vcc, v167, v159
	v_cndmask_b32_e64 v165, 0, 1, s[98:99]
	s_nop 0
	v_addc_co_u32_e32 v164, vcc, v164, v165, vcc
	s_waitcnt lgkmcnt(0)
	v_cmp_gt_f32_e64 s[16:17], v168, v159
	v_cmp_gt_f32_e32 vcc, v169, v159
	s_nop 0
	v_cndmask_b32_e64 v165, 0, 1, s[16:17]
	v_addc_co_u32_e32 v168, vcc, v164, v165, vcc
	ds_read_b128 v[164:167], v154 offset:1424
	v_cmp_gt_f32_e64 s[16:17], v170, v159
	v_cmp_gt_f32_e32 vcc, v171, v159
	s_nop 0
	v_cndmask_b32_e64 v169, 0, 1, s[16:17]
	v_addc_co_u32_e32 v172, vcc, v168, v169, vcc
	ds_read_b128 v[168:171], v154 offset:1440
	s_waitcnt lgkmcnt(1)
	v_cmp_gt_f32_e64 s[16:17], v164, v159
	v_cmp_gt_f32_e32 vcc, v165, v159
	v_cmp_gt_f32_e64 s[98:99], v166, v159
	v_cndmask_b32_e64 v164, 0, 1, s[16:17]
	v_addc_co_u32_e32 v164, vcc, v172, v164, vcc
	v_cmp_gt_f32_e32 vcc, v167, v159
	v_cndmask_b32_e64 v165, 0, 1, s[98:99]
	s_nop 0
	v_addc_co_u32_e32 v164, vcc, v164, v165, vcc
	s_waitcnt lgkmcnt(0)
	v_cmp_gt_f32_e64 s[16:17], v168, v159
	v_cmp_gt_f32_e32 vcc, v169, v159
	s_nop 0
	v_cndmask_b32_e64 v165, 0, 1, s[16:17]
	v_addc_co_u32_e32 v168, vcc, v164, v165, vcc
	ds_read_b128 v[164:167], v154 offset:1456
	v_cmp_gt_f32_e64 s[16:17], v170, v159
	v_cmp_gt_f32_e32 vcc, v171, v159
	s_nop 0
	v_cndmask_b32_e64 v169, 0, 1, s[16:17]
	v_addc_co_u32_e32 v172, vcc, v168, v169, vcc
	ds_read_b128 v[168:171], v154 offset:1472
	s_waitcnt lgkmcnt(1)
	v_cmp_gt_f32_e64 s[16:17], v164, v159
	v_cmp_gt_f32_e32 vcc, v165, v159
	v_cmp_gt_f32_e64 s[98:99], v166, v159
	v_cndmask_b32_e64 v164, 0, 1, s[16:17]
	v_addc_co_u32_e32 v164, vcc, v172, v164, vcc
	v_cmp_gt_f32_e32 vcc, v167, v159
	v_cndmask_b32_e64 v165, 0, 1, s[98:99]
	s_nop 0
	v_addc_co_u32_e32 v164, vcc, v164, v165, vcc
	s_waitcnt lgkmcnt(0)
	v_cmp_gt_f32_e64 s[16:17], v168, v159
	v_cmp_gt_f32_e32 vcc, v169, v159
	s_nop 0
	v_cndmask_b32_e64 v165, 0, 1, s[16:17]
	v_addc_co_u32_e32 v164, vcc, v164, v165, vcc
	s_nop 0
	s_nop 0
	s_nop 0
	s_nop 0
	v_cmp_gt_u32_e32 vcc, 16, v164
	v_add_u32_e32 v164, 16, v164
	s_and_b64 vcc, s[4:5], vcc
	v_cndmask_b32_e32 v168, v151, v164, vcc
	ds_read_b128 v[164:167], v154 offset:1536
	v_lshlrev_b32_e32 v168, 2, v168
	ds_permute_b32 v159, v168, v159
	ds_permute_b32 v158, v168, v158
	ds_read_b128 v[168:171], v154 offset:1552
	s_waitcnt lgkmcnt(3)
	v_cmp_gt_f32_e32 vcc, v165, v157
	s_waitcnt lgkmcnt(2)
	v_cndmask_b32_e64 v159, v163, v159, s[46:47]
	v_cndmask_b32_e64 v165, 0, 1, vcc
	v_cmp_gt_f32_e32 vcc, v164, v157
	s_waitcnt lgkmcnt(1)
	v_cndmask_b32_e64 v158, v160, v158, s[46:47]
	v_addc_co_u32_e32 v164, vcc, 0, v165, vcc
	v_cmp_gt_f32_e64 s[16:17], v166, v157
	v_cmp_gt_f32_e32 vcc, v167, v157
	s_nop 0
	v_cndmask_b32_e64 v165, 0, 1, s[16:17]
	v_addc_co_u32_e32 v164, vcc, v164, v165, vcc
	s_waitcnt lgkmcnt(0)
	v_cmp_gt_f32_e64 s[16:17], v168, v157
	v_cmp_gt_f32_e32 vcc, v169, v157
	s_nop 0
	v_cndmask_b32_e64 v165, 0, 1, s[16:17]
	v_addc_co_u32_e32 v168, vcc, v164, v165, vcc
	ds_read_b128 v[164:167], v154 offset:1568
	v_cmp_gt_f32_e64 s[16:17], v170, v157
	v_cmp_gt_f32_e32 vcc, v171, v157
	s_nop 0
	v_cndmask_b32_e64 v169, 0, 1, s[16:17]
	v_addc_co_u32_e32 v172, vcc, v168, v169, vcc
	ds_read_b128 v[168:171], v154 offset:1584
	s_waitcnt lgkmcnt(1)
	v_cmp_gt_f32_e64 s[16:17], v164, v157
	v_cmp_gt_f32_e32 vcc, v165, v157
	v_cmp_gt_f32_e64 s[98:99], v166, v157
	v_cndmask_b32_e64 v164, 0, 1, s[16:17]
	v_addc_co_u32_e32 v164, vcc, v172, v164, vcc
	v_cmp_gt_f32_e32 vcc, v167, v157
	v_cndmask_b32_e64 v165, 0, 1, s[98:99]
	s_nop 0
	v_addc_co_u32_e32 v164, vcc, v164, v165, vcc
	s_waitcnt lgkmcnt(0)
	v_cmp_gt_f32_e64 s[16:17], v168, v157
	v_cmp_gt_f32_e32 vcc, v169, v157
	s_nop 0
	v_cndmask_b32_e64 v165, 0, 1, s[16:17]
	v_addc_co_u32_e32 v168, vcc, v164, v165, vcc
	ds_read_b128 v[164:167], v154 offset:1600
	v_cmp_gt_f32_e64 s[16:17], v170, v157
	v_cmp_gt_f32_e32 vcc, v171, v157
	s_nop 0
	v_cndmask_b32_e64 v169, 0, 1, s[16:17]
	v_addc_co_u32_e32 v172, vcc, v168, v169, vcc
	ds_read_b128 v[168:171], v154 offset:1616
	s_waitcnt lgkmcnt(1)
	v_cmp_gt_f32_e64 s[16:17], v164, v157
	v_cmp_gt_f32_e32 vcc, v165, v157
	v_cmp_gt_f32_e64 s[98:99], v166, v157
	v_cndmask_b32_e64 v164, 0, 1, s[16:17]
	v_addc_co_u32_e32 v164, vcc, v172, v164, vcc
	v_cmp_gt_f32_e32 vcc, v167, v157
	v_cndmask_b32_e64 v165, 0, 1, s[98:99]
	s_nop 0
	v_addc_co_u32_e32 v164, vcc, v164, v165, vcc
	s_waitcnt lgkmcnt(0)
	v_cmp_gt_f32_e64 s[16:17], v168, v157
	v_cmp_gt_f32_e32 vcc, v169, v157
	s_nop 0
	v_cndmask_b32_e64 v165, 0, 1, s[16:17]
	v_addc_co_u32_e32 v168, vcc, v164, v165, vcc
	ds_read_b128 v[164:167], v154 offset:1632
	v_cmp_gt_f32_e64 s[16:17], v170, v157
	v_cmp_gt_f32_e32 vcc, v171, v157
	s_nop 0
	v_cndmask_b32_e64 v169, 0, 1, s[16:17]
	v_addc_co_u32_e32 v172, vcc, v168, v169, vcc
	ds_read_b128 v[168:171], v154 offset:1648
	s_waitcnt lgkmcnt(1)
	v_cmp_gt_f32_e64 s[16:17], v164, v157
	v_cmp_gt_f32_e32 vcc, v165, v157
	v_cmp_gt_f32_e64 s[98:99], v166, v157
	v_cndmask_b32_e64 v164, 0, 1, s[16:17]
	v_addc_co_u32_e32 v164, vcc, v172, v164, vcc
	v_cmp_gt_f32_e32 vcc, v167, v157
	v_cndmask_b32_e64 v165, 0, 1, s[98:99]
	s_nop 0
	v_addc_co_u32_e32 v164, vcc, v164, v165, vcc
	s_waitcnt lgkmcnt(0)
	v_cmp_gt_f32_e64 s[16:17], v168, v157
	v_cmp_gt_f32_e32 vcc, v169, v157
	s_nop 0
	v_cndmask_b32_e64 v165, 0, 1, s[16:17]
	v_addc_co_u32_e32 v168, vcc, v164, v165, vcc
	ds_read_b128 v[164:167], v154 offset:1664
	v_cmp_gt_f32_e64 s[16:17], v170, v157
	v_cmp_gt_f32_e32 vcc, v171, v157
	s_nop 0
	v_cndmask_b32_e64 v169, 0, 1, s[16:17]
	v_addc_co_u32_e32 v172, vcc, v168, v169, vcc
	ds_read_b128 v[168:171], v154 offset:1680
	s_waitcnt lgkmcnt(1)
	v_cmp_gt_f32_e64 s[16:17], v164, v157
	v_cmp_gt_f32_e32 vcc, v165, v157
	v_cmp_gt_f32_e64 s[98:99], v166, v157
	v_cndmask_b32_e64 v164, 0, 1, s[16:17]
	v_addc_co_u32_e32 v164, vcc, v172, v164, vcc
	v_cmp_gt_f32_e32 vcc, v167, v157
	v_cndmask_b32_e64 v165, 0, 1, s[98:99]
	s_nop 0
	v_addc_co_u32_e32 v164, vcc, v164, v165, vcc
	s_waitcnt lgkmcnt(0)
	v_cmp_gt_f32_e64 s[16:17], v168, v157
	v_cmp_gt_f32_e32 vcc, v169, v157
	s_nop 0
	v_cndmask_b32_e64 v165, 0, 1, s[16:17]
	v_addc_co_u32_e32 v168, vcc, v164, v165, vcc
	ds_read_b128 v[164:167], v154 offset:1696
	v_cmp_gt_f32_e64 s[16:17], v170, v157
	v_cmp_gt_f32_e32 vcc, v171, v157
	s_nop 0
	v_cndmask_b32_e64 v169, 0, 1, s[16:17]
	v_addc_co_u32_e32 v172, vcc, v168, v169, vcc
	ds_read_b128 v[168:171], v154 offset:1712
	s_waitcnt lgkmcnt(1)
	v_cmp_gt_f32_e64 s[16:17], v164, v157
	v_cmp_gt_f32_e32 vcc, v165, v157
	v_cmp_gt_f32_e64 s[98:99], v166, v157
	v_cndmask_b32_e64 v164, 0, 1, s[16:17]
	v_addc_co_u32_e32 v164, vcc, v172, v164, vcc
	v_cmp_gt_f32_e32 vcc, v167, v157
	v_cndmask_b32_e64 v165, 0, 1, s[98:99]
	s_nop 0
	v_addc_co_u32_e32 v164, vcc, v164, v165, vcc
	s_waitcnt lgkmcnt(0)
	v_cmp_gt_f32_e64 s[16:17], v168, v157
	v_cmp_gt_f32_e32 vcc, v169, v157
	s_nop 0
	v_cndmask_b32_e64 v165, 0, 1, s[16:17]
	v_addc_co_u32_e32 v168, vcc, v164, v165, vcc
	ds_read_b128 v[164:167], v154 offset:1728
	v_cmp_gt_f32_e64 s[16:17], v170, v157
	v_cmp_gt_f32_e32 vcc, v171, v157
	s_nop 0
	v_cndmask_b32_e64 v169, 0, 1, s[16:17]
	v_addc_co_u32_e32 v172, vcc, v168, v169, vcc
	ds_read_b128 v[168:171], v154 offset:1792
	s_waitcnt lgkmcnt(1)
	v_cmp_gt_f32_e64 s[16:17], v164, v157
	v_cmp_gt_f32_e32 vcc, v165, v157
	s_nop 0
	v_cndmask_b32_e64 v164, 0, 1, s[16:17]
	v_addc_co_u32_e32 v164, vcc, v172, v164, vcc
	s_nop 0
	s_nop 0
	s_nop 0
	s_nop 0
	v_cmp_gt_u32_e32 vcc, 16, v164
	v_add_u32_e32 v164, 32, v164
	s_and_b64 vcc, s[4:5], vcc
	v_cndmask_b32_e32 v164, v152, v164, vcc
	v_lshlrev_b32_e32 v164, 2, v164
	ds_permute_b32 v157, v164, v157
	s_waitcnt lgkmcnt(1)
	v_cmp_gt_f32_e32 vcc, v169, v153
	ds_permute_b32 v155, v164, v155
	ds_read_b128 v[164:167], v154 offset:1808
	s_waitcnt lgkmcnt(2)
	v_cndmask_b32_e64 v157, v159, v157, s[48:49]
	v_cndmask_b32_e64 v159, 0, 1, vcc
	v_cmp_gt_f32_e32 vcc, v168, v153
	s_waitcnt lgkmcnt(1)
	v_cndmask_b32_e64 v155, v158, v155, s[48:49]
	v_addc_co_u32_e32 v159, vcc, 0, v159, vcc
	v_cmp_gt_f32_e32 vcc, v170, v153
	s_nop 1
	v_cndmask_b32_e64 v160, 0, 1, vcc
	v_cmp_gt_f32_e32 vcc, v171, v153
	ds_read_b128 v[168:171], v154 offset:1824
	s_nop 0
	v_addc_co_u32_e32 v159, vcc, v159, v160, vcc
	s_waitcnt lgkmcnt(1)
	v_cmp_gt_f32_e64 s[16:17], v164, v153
	v_cmp_gt_f32_e32 vcc, v165, v153
	s_nop 0
	v_cndmask_b32_e64 v160, 0, 1, s[16:17]
	v_addc_co_u32_e32 v159, vcc, v159, v160, vcc
	v_cmp_gt_f32_e32 vcc, v166, v153
	s_nop 1
	v_cndmask_b32_e64 v160, 0, 1, vcc
	v_cmp_gt_f32_e32 vcc, v167, v153
	ds_read_b128 v[164:167], v154 offset:1840
	s_nop 0
	v_addc_co_u32_e32 v159, vcc, v159, v160, vcc
	s_waitcnt lgkmcnt(1)
	v_cmp_gt_f32_e64 s[16:17], v168, v153
	v_cmp_gt_f32_e32 vcc, v169, v153
	s_nop 0
	v_cndmask_b32_e64 v160, 0, 1, s[16:17]
	v_addc_co_u32_e32 v159, vcc, v159, v160, vcc
	v_cmp_gt_f32_e32 vcc, v170, v153
	s_nop 1
	v_cndmask_b32_e64 v160, 0, 1, vcc
	v_cmp_gt_f32_e32 vcc, v171, v153
	ds_read_b128 v[168:171], v154 offset:1856
	s_nop 0
	v_addc_co_u32_e32 v159, vcc, v159, v160, vcc
	s_waitcnt lgkmcnt(1)
	v_cmp_gt_f32_e64 s[16:17], v164, v153
	v_cmp_gt_f32_e32 vcc, v165, v153
	s_nop 0
	v_cndmask_b32_e64 v160, 0, 1, s[16:17]
	v_addc_co_u32_e32 v159, vcc, v159, v160, vcc
	v_cmp_gt_f32_e32 vcc, v166, v153
	s_nop 1
	v_cndmask_b32_e64 v160, 0, 1, vcc
	v_cmp_gt_f32_e32 vcc, v167, v153
	ds_read_b128 v[164:167], v154 offset:1872
	s_nop 0
	v_addc_co_u32_e32 v159, vcc, v159, v160, vcc
	s_waitcnt lgkmcnt(1)
	v_cmp_gt_f32_e64 s[16:17], v168, v153
	v_cmp_gt_f32_e32 vcc, v169, v153
	s_nop 0
	v_cndmask_b32_e64 v160, 0, 1, s[16:17]
	v_addc_co_u32_e32 v159, vcc, v159, v160, vcc
	v_cmp_gt_f32_e32 vcc, v170, v153
	s_nop 1
	v_cndmask_b32_e64 v160, 0, 1, vcc
	v_cmp_gt_f32_e32 vcc, v171, v153
	ds_read_b128 v[168:171], v154 offset:1888
	s_nop 0
	v_addc_co_u32_e32 v159, vcc, v159, v160, vcc
	s_waitcnt lgkmcnt(1)
	v_cmp_gt_f32_e64 s[16:17], v164, v153
	v_cmp_gt_f32_e32 vcc, v165, v153
	s_nop 0
	v_cndmask_b32_e64 v160, 0, 1, s[16:17]
	v_addc_co_u32_e32 v159, vcc, v159, v160, vcc
	v_cmp_gt_f32_e32 vcc, v166, v153
	s_nop 1
	v_cndmask_b32_e64 v160, 0, 1, vcc
	v_cmp_gt_f32_e32 vcc, v167, v153
	ds_read_b128 v[164:167], v154 offset:1904
	s_nop 0
	v_addc_co_u32_e32 v159, vcc, v159, v160, vcc
	s_waitcnt lgkmcnt(1)
	v_cmp_gt_f32_e64 s[16:17], v168, v153
	v_cmp_gt_f32_e32 vcc, v169, v153
	s_nop 0
	v_cndmask_b32_e64 v160, 0, 1, s[16:17]
	v_addc_co_u32_e32 v159, vcc, v159, v160, vcc
	v_cmp_gt_f32_e32 vcc, v170, v153
	s_nop 1
	v_cndmask_b32_e64 v160, 0, 1, vcc
	v_cmp_gt_f32_e32 vcc, v171, v153
	ds_read_b128 v[168:171], v154 offset:1920
	s_nop 0
	v_addc_co_u32_e32 v159, vcc, v159, v160, vcc
	s_waitcnt lgkmcnt(1)
	v_cmp_gt_f32_e64 s[16:17], v164, v153
	v_cmp_gt_f32_e32 vcc, v165, v153
	s_nop 0
	v_cndmask_b32_e64 v160, 0, 1, s[16:17]
	v_addc_co_u32_e32 v159, vcc, v159, v160, vcc
	v_cmp_gt_f32_e32 vcc, v166, v153
	s_nop 1
	v_cndmask_b32_e64 v160, 0, 1, vcc
	v_cmp_gt_f32_e32 vcc, v167, v153
	ds_read_b128 v[164:167], v154 offset:1936
	s_nop 0
	v_addc_co_u32_e32 v159, vcc, v159, v160, vcc
	s_waitcnt lgkmcnt(1)
	v_cmp_gt_f32_e64 s[16:17], v168, v153
	v_cmp_gt_f32_e32 vcc, v169, v153
	s_nop 0
	v_cndmask_b32_e64 v160, 0, 1, s[16:17]
	v_addc_co_u32_e32 v159, vcc, v159, v160, vcc
	v_cmp_gt_f32_e32 vcc, v170, v153
	s_nop 1
	v_cndmask_b32_e64 v160, 0, 1, vcc
	v_cmp_gt_f32_e32 vcc, v171, v153
	ds_read_b128 v[168:171], v154 offset:1952
	s_nop 0
	v_addc_co_u32_e32 v159, vcc, v159, v160, vcc
	s_waitcnt lgkmcnt(1)
	v_cmp_gt_f32_e64 s[16:17], v164, v153
	v_cmp_gt_f32_e32 vcc, v165, v153
	s_nop 0
	v_cndmask_b32_e64 v160, 0, 1, s[16:17]
	v_addc_co_u32_e32 v159, vcc, v159, v160, vcc
	v_cmp_gt_f32_e32 vcc, v166, v153
	s_nop 1
	v_cndmask_b32_e64 v160, 0, 1, vcc
	v_cmp_gt_f32_e32 vcc, v167, v153
	ds_read_b128 v[164:167], v154 offset:1968
	s_nop 0
	v_addc_co_u32_e32 v159, vcc, v159, v160, vcc
	s_waitcnt lgkmcnt(1)
	v_cmp_gt_f32_e64 s[16:17], v168, v153
	v_cmp_gt_f32_e32 vcc, v169, v153
	s_nop 0
	v_cndmask_b32_e64 v160, 0, 1, s[16:17]
	v_addc_co_u32_e32 v159, vcc, v159, v160, vcc
	v_cmp_gt_f32_e32 vcc, v170, v153
	s_nop 1
	v_cndmask_b32_e64 v160, 0, 1, vcc
	v_cmp_gt_f32_e32 vcc, v171, v153
	ds_read_b128 v[168:171], v154 offset:1984
	s_nop 0
	v_addc_co_u32_e32 v159, vcc, v159, v160, vcc
	s_waitcnt lgkmcnt(1)
	v_cmp_gt_f32_e32 vcc, v164, v153
	v_max_f32_e32 v160, v162, v162
	s_nop 0
	v_cndmask_b32_e64 v154, 0, 1, vcc
	v_cmp_gt_f32_e32 vcc, v165, v153
	s_nop 1
	v_addc_co_u32_e32 v154, vcc, v159, v154, vcc
	v_cmp_gt_f32_e64 s[16:17], v166, v153
	v_cmp_gt_f32_e32 vcc, v167, v153
	s_nop 0
	v_cndmask_b32_e64 v159, 0, 1, s[16:17]
	v_addc_co_u32_e32 v154, vcc, v154, v159, vcc
	s_waitcnt lgkmcnt(0)
	v_cmp_gt_f32_e64 s[16:17], v168, v153
	v_cmp_gt_f32_e32 vcc, v169, v153
	s_nop 0
	v_cndmask_b32_e64 v159, 0, 1, s[16:17]
	v_addc_co_u32_e32 v154, vcc, v154, v159, vcc
	s_nop 0
	s_nop 0
	s_nop 0
	s_nop 0
	v_mov_b32_e32 v159, v201
	v_cmp_gt_u32_e32 vcc, 16, v154
	v_add_u32_e32 v154, 48, v154
	v_mov_b32_dpp v159, v162 row_ror:1 row_mask:0xf bank_mask:0xf
	v_max_f32_e32 v159, v159, v159
	v_max_f32_e32 v159, v160, v159
	v_mov_b32_e32 v160, v201
	s_and_b64 vcc, s[4:5], vcc
	v_cndmask_b32_e32 v154, v140, v154, vcc
	v_mov_b32_dpp v160, v159 row_ror:2 row_mask:0xf bank_mask:0xf
	v_max_f32_e32 v160, v160, v160
	v_max_f32_e32 v159, v159, v160
	v_mov_b32_e32 v160, v201
	v_lshlrev_b32_e32 v154, 2, v154
	ds_permute_b32 v153, v154, v153
	v_mov_b32_dpp v160, v159 row_ror:4 row_mask:0xf bank_mask:0xf
	v_max_f32_e32 v160, v160, v160
	v_max_f32_e32 v159, v159, v160
	v_mov_b32_e32 v160, v201
	ds_permute_b32 v154, v154, v156
	s_waitcnt lgkmcnt(1)
	v_cndmask_b32_e64 v153, v157, v153, s[50:51]
	v_mov_b32_dpp v160, v159 row_ror:8 row_mask:0xf bank_mask:0xf
	v_max_f32_e32 v160, v160, v160
	v_max_f32_e32 v159, v159, v160
	v_sub_f32_e32 v159, v162, v159
	v_mul_f32_e32 v159, 0x3fb8aa3b, v159
	v_exp_f32_e32 v159, v159
	s_waitcnt lgkmcnt(0)
	v_cndmask_b32_e64 v158, v155, v154, s[50:51]
	v_add_f32_dpp v156, v159, v159 row_ror:1 row_mask:0xf bank_mask:0xf bound_ctrl:1
	s_nop 1
	v_add_f32_dpp v156, v156, v156 row_ror:2 row_mask:0xf bank_mask:0xf bound_ctrl:1
	s_nop 1
	v_add_f32_dpp v156, v156, v156 row_ror:4 row_mask:0xf bank_mask:0xf bound_ctrl:1
	s_nop 1
	v_add_f32_dpp v156, v156, v156 row_ror:8 row_mask:0xf bank_mask:0xf bound_ctrl:1
	v_div_scale_f32 v160, s[80:81], v156, v156, v159
	v_rcp_f32_e32 v162, v160
	s_mov_b32 s80, 0x31200000
	v_fma_f32 v154, -v160, v162, 1.0
	v_fmac_f32_e32 v162, v154, v162
	v_div_scale_f32 v154, vcc, v159, v156, v159
	v_mul_f32_e32 v155, v154, v162
	v_fma_f32 v157, -v160, v155, v154
	v_fmac_f32_e32 v155, v157, v162
	v_fma_f32 v154, -v160, v155, v154
	v_mov_b32_e32 v157, v201
	v_div_fmas_f32 v154, v154, v162, v155
	v_div_fixup_f32 v156, v154, v156, v159
	v_mov_b32_dpp v157, v153 row_ror:1 row_mask:0xf bank_mask:0xf
	v_max_f32_e32 v159, v153, v153
	v_max_f32_e32 v157, v157, v157
	v_max_f32_e32 v157, v159, v157
	v_mov_b32_e32 v159, v201
	v_lshl_add_u64 v[154:155], s[92:93], 0, v[132:133]
	v_add_co_u32_e32 v154, vcc, s80, v154
	v_mov_b32_dpp v159, v157 row_ror:2 row_mask:0xf bank_mask:0xf
	v_max_f32_e32 v159, v159, v159
	v_max_f32_e32 v157, v157, v159
	v_mov_b32_e32 v159, v201
	v_addc_co_u32_e32 v155, vcc, 0, v155, vcc
	s_nop 0
	v_mov_b32_dpp v159, v157 row_ror:4 row_mask:0xf bank_mask:0xf
	v_max_f32_e32 v159, v159, v159
	v_max_f32_e32 v157, v157, v159
	v_mov_b32_e32 v159, v201
	global_store_dword v[154:155], v156, off
	s_nop 0
	v_mov_b32_dpp v159, v157 row_ror:8 row_mask:0xf bank_mask:0xf
	v_max_f32_e32 v159, v159, v159
	v_max_f32_e32 v157, v157, v159
	v_sub_f32_e32 v153, v153, v157
	v_mul_f32_e32 v153, 0x3fb8aa3b, v153
	v_exp_f32_e32 v153, v153
	s_nop 1
	v_add_f32_dpp v156, v153, v153 row_ror:1 row_mask:0xf bank_mask:0xf bound_ctrl:1
	s_nop 1
	v_add_f32_dpp v156, v156, v156 row_ror:2 row_mask:0xf bank_mask:0xf bound_ctrl:1
	s_nop 1
	v_add_f32_dpp v156, v156, v156 row_ror:4 row_mask:0xf bank_mask:0xf bound_ctrl:1
	s_nop 1
	v_add_f32_dpp v159, v156, v156 row_ror:8 row_mask:0xf bank_mask:0xf bound_ctrl:1
	v_div_scale_f32 v160, s[80:81], v159, v159, v153
	v_rcp_f32_e32 v162, v160
	v_lshl_add_u64 v[156:157], s[92:93], 0, v[134:135]
	global_store_dword v[156:157], v161, off
	v_fma_f32 v156, -v160, v162, 1.0
	v_fmac_f32_e32 v162, v156, v162
	v_div_scale_f32 v156, vcc, v153, v159, v153
	v_mul_f32_e32 v157, v156, v162
	v_fma_f32 v161, -v160, v157, v156
	v_fmac_f32_e32 v157, v161, v162
	v_fma_f32 v156, -v160, v157, v156
	v_div_fmas_f32 v156, v156, v162, v157
	v_div_fixup_f32 v153, v156, v159, v153
	global_store_dword v[154:155], v153, off offset:256
	v_lshlrev_b32_e32 v153, 7, v158
	v_lshl_add_u64 v[154:155], s[92:93], 0, v[136:137]
	s_and_b64 vcc, exec, s[52:53]
	global_store_dword v[154:155], v153, off
	s_cbranch_vccnz .LBB0_1847
	v_readlane_b32 s10, v254, 10
	v_readlane_b32 s11, v254, 11
	s_andn2_b64 vcc, exec, s[10:11]
	s_cbranch_vccnz .LBB0_1871
	global_load_dwordx4 v[164:167], v[112:113], off
	global_load_dwordx4 v[168:171], v[112:113], off offset:16
	global_load_dwordx4 v[172:175], v[112:113], off offset:32
	global_load_dwordx4 v[176:179], v[112:113], off offset:48
	global_load_dwordx4 v[180:183], v[114:115], off
	global_load_dwordx4 v[184:187], v[116:117], off
	global_load_dwordx4 v[188:191], v[118:119], off
	global_load_dwordx4 v[192:195], v[120:121], off
	s_waitcnt vmcnt(0)
	v_pk_mul_f32 v[46:47], v[46:47], v[166:167]
	v_pk_mul_f32 v[44:45], v[44:45], v[164:165]
	v_pk_mul_f32 v[42:43], v[42:43], v[170:171]
	v_pk_mul_f32 v[40:41], v[40:41], v[168:169]
	v_pk_mul_f32 v[38:39], v[38:39], v[174:175]
	v_pk_mul_f32 v[36:37], v[36:37], v[172:173]
	v_pk_mul_f32 v[34:35], v[34:35], v[178:179]
	v_pk_mul_f32 v[32:33], v[32:33], v[176:177]
	v_pk_mul_f32 v[50:51], v[50:51], v[182:183]
	v_pk_mul_f32 v[48:49], v[48:49], v[180:181]
	v_pk_mul_f32 v[62:63], v[62:63], v[186:187]
	v_pk_mul_f32 v[60:61], v[60:61], v[184:185]
	v_pk_mul_f32 v[58:59], v[58:59], v[190:191]
	v_pk_mul_f32 v[56:57], v[56:57], v[188:189]
	v_pk_mul_f32 v[54:55], v[54:55], v[194:195]
	v_pk_mul_f32 v[52:53], v[52:53], v[192:193]
.LBB0_1871:
	s_waitcnt vmcnt(16)
	v_max_f32_e64 v153, |v47|, |v47|
	v_max_f32_e64 v154, |v46|, |v46|
	v_max_f32_e32 v153, v154, v153
	v_max_f32_e64 v154, |v43|, |v43|
	v_max_f32_e64 v155, |v42|, |v42|
	v_max_f32_e32 v154, v155, v154
	v_max3_f32 v153, |v44|, |v45|, v153
	v_max3_f32 v154, |v40|, |v41|, v154
	v_max3_f32 v153, v153, 0, v154
	v_max_f32_e64 v154, |v39|, |v39|
	v_max_f32_e64 v155, |v38|, |v38|
	v_max_f32_e32 v154, v155, v154
	v_max_f32_e64 v155, |v35|, |v35|
	v_max_f32_e64 v156, |v34|, |v34|
	v_max_f32_e32 v155, v156, v155
	v_max3_f32 v154, |v36|, |v37|, v154
	v_max3_f32 v155, |v32|, |v33|, v155
	v_max3_f32 v153, v153, v154, v155
	s_waitcnt vmcnt(15)
	v_max_f32_e64 v154, |v51|, |v51|
	v_max_f32_e64 v155, |v50|, |v50|
	v_max_f32_e32 v154, v155, v154
	s_waitcnt vmcnt(12)
	v_max_f32_e64 v155, |v63|, |v63|
	v_max_f32_e64 v156, |v62|, |v62|
	v_max_f32_e32 v155, v156, v155
	v_max3_f32 v154, |v48|, |v49|, v154
	v_max3_f32 v155, |v60|, |v61|, v155
	v_max3_f32 v153, v153, v154, v155
	v_max_f32_e64 v154, |v59|, |v59|
	v_max_f32_e64 v155, |v58|, |v58|
	v_max_f32_e32 v154, v155, v154
	v_max_f32_e64 v155, |v55|, |v55|
	v_max_f32_e64 v156, |v54|, |v54|
	v_max_f32_e32 v155, v156, v155
	v_max3_f32 v154, |v56|, |v57|, v154
	v_max3_f32 v155, |v52|, |v53|, v155
	v_max3_f32 v153, v153, v154, v155
	v_mov_b32_e32 v154, v201
	s_mov_b32 s9, 0x42fe0000
	s_nop 0
	v_mov_b32_dpp v154, v153 row_ror:1 row_mask:0xf bank_mask:0xf
	v_max_f32_e32 v154, v154, v154
	v_max_f32_e32 v153, v153, v154
	v_mov_b32_e32 v154, v201
	s_nop 1
	v_mov_b32_dpp v154, v153 row_ror:2 row_mask:0xf bank_mask:0xf
	v_max_f32_e32 v154, v154, v154
	v_max_f32_e32 v153, v153, v154
	v_mov_b32_e32 v154, v201
	s_nop 1
	v_mov_b32_dpp v154, v153 row_ror:4 row_mask:0xf bank_mask:0xf
	v_max_f32_e32 v154, v154, v154
	v_max_f32_e32 v153, v153, v154
	v_mov_b32_e32 v154, v201
	s_nop 1
	v_mov_b32_dpp v154, v153 row_ror:8 row_mask:0xf bank_mask:0xf
	v_max_f32_e32 v154, v154, v154
	v_max_f32_e32 v153, v153, v154
	v_mov_b32_e32 v154, v153
	s_nop 1
	v_permlane16_swap_b32_e32 v153, v154
	v_max_f32_e32 v154, v154, v154
	v_max_f32_e32 v153, v153, v153
	v_max_f32_e32 v153, v153, v154
	v_mov_b32_e32 v154, v153
	s_nop 1
	v_permlane32_swap_b32_e32 v153, v154
	v_max_f32_e32 v154, v154, v154
	v_max_f32_e32 v153, v153, v153
	v_max_f32_e32 v153, v153, v154
	v_div_scale_f32 v154, s[52:53], v153, v153, s9
	v_rcp_f32_e32 v155, v154
	s_add_u32 s52, s92, s74
	s_addc_u32 s53, s93, s75
	v_fma_f32 v156, -v154, v155, 1.0
	v_fmac_f32_e32 v155, v156, v155
	v_div_scale_f32 v156, vcc, s9, v153, s9
	v_mul_f32_e32 v157, v156, v155
	v_fma_f32 v158, -v154, v157, v156
	v_fmac_f32_e32 v157, v158, v155
	v_fma_f32 v154, -v154, v157, v156
	v_div_fmas_f32 v154, v154, v155, v157
	v_div_fixup_f32 v154, v154, v153, s9
	v_cmp_lt_f32_e32 vcc, 0, v153
	s_mov_b32 s9, 0x40c0c00
	s_nop 0
	v_cndmask_b32_e32 v158, 0, v154, vcc
	v_pk_mul_f32 v[156:157], v[44:45], v[158:159] op_sel_hi:[1,0]
	v_pk_mul_f32 v[154:155], v[46:47], v[158:159] op_sel_hi:[1,0]
	v_pk_add_f32 v[156:157], v[156:157], v[242:243] op_sel_hi:[1,0]
	s_nop 0
	v_pk_add_f32 v[154:155], v[154:155], v[242:243] op_sel_hi:[1,0]
	v_perm_b32 v155, v155, v156, s9
	v_pk_mul_f32 v[160:161], v[40:41], v[158:159] op_sel_hi:[1,0]
	v_perm_b32 v230, v157, v155, v226
	v_perm_b32 v154, v154, v230, v228
	v_pk_mul_f32 v[156:157], v[42:43], v[158:159] op_sel_hi:[1,0]
	v_add_f32_e32 v159, 0x4b400000, v161
	v_add_f32_e32 v155, 0x4b400000, v160
	v_pk_add_f32 v[156:157], v[156:157], v[242:243] op_sel_hi:[1,0]
	v_perm_b32 v155, v157, v155, s9
	v_pk_mul_f32 v[160:161], v[36:37], v[158:159] op_sel_hi:[1,0]
	v_perm_b32 v230, v159, v155, v226
	v_perm_b32 v155, v156, v230, v228
	v_pk_mul_f32 v[156:157], v[38:39], v[158:159] op_sel_hi:[1,0]
	v_add_f32_e32 v159, 0x4b400000, v160
	v_add_f32_e32 v160, 0x4b400000, v161
	v_pk_add_f32 v[156:157], v[156:157], v[242:243] op_sel_hi:[1,0]
	v_perm_b32 v157, v157, v159, s9
	v_pk_mul_f32 v[162:163], v[32:33], v[158:159] op_sel_hi:[1,0]
	v_perm_b32 v230, v160, v157, v226
	v_perm_b32 v156, v156, v230, v228
	v_pk_mul_f32 v[160:161], v[34:35], v[158:159] op_sel_hi:[1,0]
	v_add_f32_e32 v159, 0x4b400000, v163
	v_add_f32_e32 v157, 0x4b400000, v162
	v_pk_add_f32 v[160:161], v[160:161], v[242:243] op_sel_hi:[1,0]
	s_nop 0
	v_perm_b32 v157, v161, v157, s9
	v_perm_b32 v230, v159, v157, v226
	v_perm_b32 v157, v160, v230, v228
	v_lshl_add_u64 v[160:161], v[130:131], 0, v[200:201]
	global_store_dwordx4 v[160:161], v[154:157], off
	v_pk_mul_f32 v[160:161], v[60:61], v[158:159] op_sel_hi:[1,0]
	s_nop 0
	v_pk_mul_f32 v[156:157], v[48:49], v[158:159] op_sel_hi:[1,0]
	v_pk_mul_f32 v[154:155], v[50:51], v[158:159] op_sel_hi:[1,0]
	v_pk_add_f32 v[156:157], v[156:157], v[242:243] op_sel_hi:[1,0]
	s_nop 0
	v_pk_add_f32 v[154:155], v[154:155], v[242:243] op_sel_hi:[1,0]
	v_perm_b32 v155, v155, v156, s9
	v_perm_b32 v230, v157, v155, v226
	v_perm_b32 v154, v154, v230, v228
	v_pk_mul_f32 v[156:157], v[62:63], v[158:159] op_sel_hi:[1,0]
	v_add_f32_e32 v159, 0x4b400000, v161
	v_add_f32_e32 v155, 0x4b400000, v160
	v_pk_add_f32 v[156:157], v[156:157], v[242:243] op_sel_hi:[1,0]
	v_perm_b32 v155, v157, v155, s9
	v_pk_mul_f32 v[160:161], v[56:57], v[158:159] op_sel_hi:[1,0]
	v_perm_b32 v230, v159, v155, v226
	v_perm_b32 v155, v156, v230, v228
	v_pk_mul_f32 v[156:157], v[58:59], v[158:159] op_sel_hi:[1,0]
	v_add_f32_e32 v159, 0x4b400000, v160
	v_add_f32_e32 v160, 0x4b400000, v161
	v_pk_add_f32 v[156:157], v[156:157], v[242:243] op_sel_hi:[1,0]
	s_nop 0
	s_nop 0
	v_perm_b32 v157, v157, v159, s9
	v_perm_b32 v230, v160, v157, v226
	v_perm_b32 v156, v156, v230, v228
	v_pk_mul_f32 v[160:161], v[54:55], v[158:159] op_sel_hi:[1,0]
	v_pk_mul_f32 v[158:159], v[52:53], v[158:159] op_sel_hi:[1,0]
	s_nop 0
	v_add_f32_e32 v157, 0x4b400000, v158
	v_add_f32_e32 v158, 0x4b400000, v159
	s_nop 0
	v_add_f32_e32 v159, 0x4b400000, v160
	v_add_f32_e32 v160, 0x4b400000, v161
	s_nop 0
	s_nop 0
	s_nop 0
	v_perm_b32 v157, v160, v157, s9
	v_perm_b32 v230, v158, v157, v226
	v_perm_b32 v157, v159, v230, v228
	v_lshl_add_u64 v[158:159], v[128:129], 0, v[200:201]
	global_store_dwordx4 v[158:159], v[154:157], off
	s_and_saveexec_b64 s[80:81], s[20:21]
	s_cbranch_execz .LBB0_1873
	v_mul_f32_e32 v153, 0x3c010204, v153
	v_mov_b32_e32 v154, 0x850000
	global_store_dword v154, v153, s[52:53]
.LBB0_1873:
	s_or_b64 exec, exec, s[80:81]
	s_waitcnt vmcnt(13)
	v_max_f32_e64 v153, |v67|, |v67|
	v_max_f32_e64 v154, |v66|, |v66|
	v_max_f32_e32 v153, v154, v153
	s_waitcnt vmcnt(10)
	v_max_f32_e64 v154, |v79|, |v79|
	v_max_f32_e64 v155, |v78|, |v78|
	v_max_f32_e32 v154, v155, v154
	v_max3_f32 v153, |v64|, |v65|, v153
	v_max3_f32 v154, |v76|, |v77|, v154
	v_max3_f32 v153, v153, 0, v154
	v_max_f32_e64 v154, |v75|, |v75|
	v_max_f32_e64 v155, |v74|, |v74|
	v_max_f32_e32 v154, v155, v154
	v_max_f32_e64 v155, |v71|, |v71|
	v_max_f32_e64 v156, |v70|, |v70|
	v_max_f32_e32 v155, v156, v155
	v_max3_f32 v154, |v72|, |v73|, v154
	v_max3_f32 v155, |v68|, |v69|, v155
	v_max3_f32 v153, v153, v154, v155
	s_waitcnt vmcnt(9)
	v_max_f32_e64 v154, |v83|, |v83|
	v_max_f32_e64 v155, |v82|, |v82|
	v_max_f32_e32 v154, v155, v154
	s_waitcnt vmcnt(6)
	v_max_f32_e64 v155, |v95|, |v95|
	v_max_f32_e64 v156, |v94|, |v94|
	v_max_f32_e32 v155, v156, v155
	v_max3_f32 v154, |v80|, |v81|, v154
	v_max3_f32 v155, |v92|, |v93|, v155
	v_max3_f32 v153, v153, v154, v155
	v_max_f32_e64 v154, |v91|, |v91|
	v_max_f32_e64 v155, |v90|, |v90|
	v_max_f32_e32 v154, v155, v154
	v_max_f32_e64 v155, |v87|, |v87|
	v_max_f32_e64 v156, |v86|, |v86|
	v_max_f32_e32 v155, v156, v155
	v_max3_f32 v154, |v88|, |v89|, v154
	v_max3_f32 v155, |v84|, |v85|, v155
	v_max3_f32 v153, v153, v154, v155
	v_mov_b32_e32 v154, v201
	s_mov_b32 s9, 0x42fe0000
	s_nop 0
	v_mov_b32_dpp v154, v153 row_ror:1 row_mask:0xf bank_mask:0xf
	v_max_f32_e32 v154, v154, v154
	v_max_f32_e32 v153, v153, v154
	v_mov_b32_e32 v154, v201
	s_nop 1
	v_mov_b32_dpp v154, v153 row_ror:2 row_mask:0xf bank_mask:0xf
	v_max_f32_e32 v154, v154, v154
	v_max_f32_e32 v153, v153, v154
	v_mov_b32_e32 v154, v201
	s_nop 1
	v_mov_b32_dpp v154, v153 row_ror:4 row_mask:0xf bank_mask:0xf
	v_max_f32_e32 v154, v154, v154
	v_max_f32_e32 v153, v153, v154
	v_mov_b32_e32 v154, v201
	s_nop 1
	v_mov_b32_dpp v154, v153 row_ror:8 row_mask:0xf bank_mask:0xf
	v_max_f32_e32 v154, v154, v154
	v_max_f32_e32 v153, v153, v154
	v_mov_b32_e32 v154, v153
	s_nop 1
	v_permlane16_swap_b32_e32 v153, v154
	v_max_f32_e32 v154, v154, v154
	v_max_f32_e32 v153, v153, v153
	v_max_f32_e32 v153, v153, v154
	v_mov_b32_e32 v154, v153
	s_nop 1
	v_permlane32_swap_b32_e32 v153, v154
	v_max_f32_e32 v154, v154, v154
	v_max_f32_e32 v153, v153, v153
	v_max_f32_e32 v153, v153, v154
	v_div_scale_f32 v154, s[80:81], v153, v153, s9
	v_rcp_f32_e32 v155, v154
	s_nop 0
	v_fma_f32 v156, -v154, v155, 1.0
	v_fmac_f32_e32 v155, v156, v155
	v_div_scale_f32 v156, vcc, s9, v153, s9
	v_mul_f32_e32 v157, v156, v155
	v_fma_f32 v158, -v154, v157, v156
	v_fmac_f32_e32 v157, v158, v155
	v_fma_f32 v154, -v154, v157, v156
	v_div_fmas_f32 v154, v154, v155, v157
	v_div_fixup_f32 v154, v154, v153, s9
	v_cmp_lt_f32_e32 vcc, 0, v153
	s_mov_b32 s9, 0x40c0c00
	s_nop 0
	v_cndmask_b32_e32 v158, 0, v154, vcc
	v_pk_mul_f32 v[156:157], v[64:65], v[158:159] op_sel_hi:[1,0]
	v_pk_mul_f32 v[154:155], v[66:67], v[158:159] op_sel_hi:[1,0]
	v_pk_add_f32 v[156:157], v[156:157], v[242:243] op_sel_hi:[1,0]
	s_nop 0
	v_pk_add_f32 v[154:155], v[154:155], v[242:243] op_sel_hi:[1,0]
	v_perm_b32 v155, v155, v156, s9
	v_pk_mul_f32 v[160:161], v[76:77], v[158:159] op_sel_hi:[1,0]
	v_perm_b32 v230, v157, v155, v226
	v_perm_b32 v154, v154, v230, v228
	v_pk_mul_f32 v[156:157], v[78:79], v[158:159] op_sel_hi:[1,0]
	v_add_f32_e32 v159, 0x4b400000, v161
	v_add_f32_e32 v155, 0x4b400000, v160
	v_pk_add_f32 v[156:157], v[156:157], v[242:243] op_sel_hi:[1,0]
	v_perm_b32 v155, v157, v155, s9
	v_pk_mul_f32 v[160:161], v[72:73], v[158:159] op_sel_hi:[1,0]
	v_perm_b32 v230, v159, v155, v226
	v_perm_b32 v155, v156, v230, v228
	v_pk_mul_f32 v[156:157], v[74:75], v[158:159] op_sel_hi:[1,0]
	v_add_f32_e32 v159, 0x4b400000, v160
	v_add_f32_e32 v160, 0x4b400000, v161
	v_pk_add_f32 v[156:157], v[156:157], v[242:243] op_sel_hi:[1,0]
	v_perm_b32 v157, v157, v159, s9
	v_pk_mul_f32 v[162:163], v[68:69], v[158:159] op_sel_hi:[1,0]
	v_perm_b32 v230, v160, v157, v226
	v_perm_b32 v156, v156, v230, v228
	v_pk_mul_f32 v[160:161], v[70:71], v[158:159] op_sel_hi:[1,0]
	v_add_f32_e32 v159, 0x4b400000, v163
	v_add_f32_e32 v157, 0x4b400000, v162
	v_pk_add_f32 v[160:161], v[160:161], v[242:243] op_sel_hi:[1,0]
	s_nop 0
	v_perm_b32 v157, v161, v157, s9
	v_perm_b32 v230, v159, v157, v226
	v_perm_b32 v157, v160, v230, v228
	v_lshl_add_u64 v[160:161], v[126:127], 0, v[200:201]
	global_store_dwordx4 v[160:161], v[154:157], off
	v_pk_mul_f32 v[160:161], v[92:93], v[158:159] op_sel_hi:[1,0]
	s_nop 0
	v_pk_mul_f32 v[156:157], v[80:81], v[158:159] op_sel_hi:[1,0]
	v_pk_mul_f32 v[154:155], v[82:83], v[158:159] op_sel_hi:[1,0]
	v_pk_add_f32 v[156:157], v[156:157], v[242:243] op_sel_hi:[1,0]
	s_nop 0
	v_pk_add_f32 v[154:155], v[154:155], v[242:243] op_sel_hi:[1,0]
	v_perm_b32 v155, v155, v156, s9
	v_perm_b32 v230, v157, v155, v226
	v_perm_b32 v154, v154, v230, v228
	v_pk_mul_f32 v[156:157], v[94:95], v[158:159] op_sel_hi:[1,0]
	v_add_f32_e32 v159, 0x4b400000, v161
	v_add_f32_e32 v155, 0x4b400000, v160
	v_pk_add_f32 v[156:157], v[156:157], v[242:243] op_sel_hi:[1,0]
	v_perm_b32 v155, v157, v155, s9
	v_pk_mul_f32 v[160:161], v[88:89], v[158:159] op_sel_hi:[1,0]
	v_perm_b32 v230, v159, v155, v226
	v_perm_b32 v155, v156, v230, v228
	v_pk_mul_f32 v[156:157], v[90:91], v[158:159] op_sel_hi:[1,0]
	v_add_f32_e32 v159, 0x4b400000, v160
	v_add_f32_e32 v160, 0x4b400000, v161
	v_pk_add_f32 v[156:157], v[156:157], v[242:243] op_sel_hi:[1,0]
	s_nop 0
	s_nop 0
	v_perm_b32 v157, v157, v159, s9
	v_perm_b32 v230, v160, v157, v226
	v_perm_b32 v156, v156, v230, v228
	v_pk_mul_f32 v[160:161], v[86:87], v[158:159] op_sel_hi:[1,0]
	v_pk_mul_f32 v[158:159], v[84:85], v[158:159] op_sel_hi:[1,0]
	s_nop 0
	v_add_f32_e32 v157, 0x4b400000, v158
	v_add_f32_e32 v158, 0x4b400000, v159
	s_nop 0
	v_add_f32_e32 v159, 0x4b400000, v160
	v_add_f32_e32 v160, 0x4b400000, v161
	s_nop 0
	s_nop 0
	s_nop 0
	v_perm_b32 v157, v160, v157, s9
	v_perm_b32 v230, v158, v157, v226
	v_perm_b32 v157, v159, v230, v228
	v_lshl_add_u64 v[158:159], v[124:125], 0, v[200:201]
	global_store_dwordx4 v[158:159], v[154:157], off
	s_and_saveexec_b64 s[80:81], s[20:21]
	s_cbranch_execz .LBB0_1846
	v_mul_f32_e32 v153, 0x3c010204, v153
	v_mov_b32_e32 v154, 0x890000
	global_store_dword v154, v153, s[52:53]
	s_branch .LBB0_1846
